# attention: waves 0-3 skip the final key step and the drain of each unit (both tiles are fully masked for their rows, P = 0 exactly); placement as v052
# speedup vs baseline: 1.0121x; 1.0084x over previous
.LBB0_339:
	s_cmp_lt_u32 s83, 4
	s_cbranch_scc1 .Lfin_skip_l0
	v_add_u32_e32 v2, s33, v242
	ds_read_b64_tr_b16 v[194:195], v2 offset:24576
	ds_read_b64_tr_b16 v[196:197], v2 offset:25088
	s_waitcnt lgkmcnt(9)
	v_mfma_f32_32x32x16_bf16 v[82:97], v[170:173], v[154:157], v[100:115]
	ds_read_b64_tr_b16 v[170:171], v2 offset:28672
	ds_read_b64_tr_b16 v[172:173], v2 offset:29184
	s_waitcnt lgkmcnt(10)
	v_mfma_f32_32x32x16_bf16 v[100:115], v[162:165], v[154:157], v[100:115]
	ds_read_b64_tr_b16 v[124:125], v2 offset:25600
	ds_read_b64_tr_b16 v[126:127], v2 offset:26112
	s_waitcnt lgkmcnt(11)
	v_mfma_f32_32x32x16_bf16 v[82:97], v[174:177], v[150:153], v[82:97]
	ds_read_b64_tr_b16 v[120:121], v2 offset:29696
	ds_read_b64_tr_b16 v[122:123], v2 offset:30208
	s_waitcnt lgkmcnt(12)
	v_mfma_f32_32x32x16_bf16 v[100:115], v[166:169], v[150:153], v[100:115]
	ds_read_b64_tr_b16 v[116:117], v2 offset:26624
	ds_read_b64_tr_b16 v[118:119], v2 offset:27136
	s_waitcnt lgkmcnt(13)
	v_mfma_f32_32x32x16_bf16 v[82:97], v[182:185], v[146:149], v[82:97]
	ds_read_b64_tr_b16 v[12:13], v2 offset:30720
	ds_read_b64_tr_b16 v[14:15], v2 offset:31232
	s_waitcnt lgkmcnt(14)
	v_mfma_f32_32x32x16_bf16 v[100:115], v[178:181], v[146:149], v[100:115]
	ds_read_b64_tr_b16 v[8:9], v2 offset:27648
	ds_read_b64_tr_b16 v[10:11], v2 offset:28160
	s_waitcnt lgkmcnt(14)
	v_mfma_f32_32x32x16_bf16 v[82:97], v[190:193], v[142:145], v[82:97]
	ds_read_b64_tr_b16 v[4:5], v2 offset:31744
	ds_read_b64_tr_b16 v[6:7], v2 offset:32256
	v_mfma_f32_32x32x16_bf16 v[100:115], v[186:189], v[142:145], v[100:115]
	v_or_b32_e32 v17, 0xe0, v239
	v_or_b32_e32 v16, 0xc0, v239
	v_cmp_le_i32_e32 vcc, v17, v238
	s_nop 8
	v_cndmask_b32_e32 v99, v227, v100, vcc
	v_cmp_lt_i32_e32 vcc, v16, v238
	s_nop 1
	v_cndmask_b32_e32 v83, v227, v83, vcc
	v_cmp_le_i32_e32 vcc, v16, v238
	v_or_b32_e32 v16, 0xe1, v239
	s_nop 0
	v_cndmask_b32_e32 v82, v227, v82, vcc
	v_cmp_le_i32_e32 vcc, v16, v238
	v_or_b32_e32 v16, 0xc2, v239
	s_nop 0
	v_cndmask_b32_e32 v100, v227, v101, vcc
	v_cmp_le_i32_e32 vcc, v16, v238
	v_or_b32_e32 v16, 0xe2, v239
	s_nop 0
	v_cndmask_b32_e32 v101, v227, v84, vcc
	v_cmp_le_i32_e32 vcc, v16, v238
	v_or_b32_e32 v16, 0xc3, v239
	s_nop 0
	v_cndmask_b32_e32 v142, v227, v102, vcc
	v_cmp_le_i32_e32 vcc, v16, v238
	v_or_b32_e32 v16, 0xe3, v239
	s_nop 0
	v_cndmask_b32_e32 v143, v227, v85, vcc
	v_cmp_le_i32_e32 vcc, v16, v238
	v_or_b32_e32 v16, 0xc8, v239
	s_nop 0
	v_cndmask_b32_e32 v144, v227, v103, vcc
	v_cmp_le_i32_e32 vcc, v16, v238
	v_or_b32_e32 v16, 0xe8, v239
	s_nop 0
	v_cndmask_b32_e32 v102, v227, v86, vcc
	v_cmp_le_i32_e32 vcc, v16, v238
	v_or_b32_e32 v16, 0xc9, v239
	s_nop 0
	v_cndmask_b32_e32 v86, v227, v104, vcc
	v_cmp_le_i32_e32 vcc, v16, v238
	v_or_b32_e32 v16, 0xe9, v239
	s_nop 0
	v_cndmask_b32_e32 v103, v227, v87, vcc
	v_cmp_le_i32_e32 vcc, v16, v238
	v_or_b32_e32 v16, 0xca, v239
	s_nop 0
	v_cndmask_b32_e32 v87, v227, v105, vcc
	v_cmp_le_i32_e32 vcc, v16, v238
	v_or_b32_e32 v16, 0xea, v239
	s_nop 0
	v_cndmask_b32_e32 v104, v227, v88, vcc
	v_cmp_le_i32_e32 vcc, v16, v238
	v_or_b32_e32 v16, 0xcb, v239
	s_nop 0
	v_cndmask_b32_e32 v88, v227, v106, vcc
	v_cmp_le_i32_e32 vcc, v16, v238
	v_or_b32_e32 v16, 0xeb, v239
	s_nop 0
	v_cndmask_b32_e32 v105, v227, v89, vcc
	v_cmp_le_i32_e32 vcc, v16, v238
	v_or_b32_e32 v16, 0xd0, v239
	s_nop 0
	v_cndmask_b32_e32 v89, v227, v107, vcc
	v_cmp_le_i32_e32 vcc, v16, v238
	v_or_b32_e32 v16, 0xf0, v239
	s_nop 0
	v_cndmask_b32_e32 v106, v227, v90, vcc
	v_cmp_le_i32_e32 vcc, v16, v238
	v_or_b32_e32 v16, 0xd1, v239
	s_nop 0
	v_cndmask_b32_e32 v90, v227, v108, vcc
	v_cmp_le_i32_e32 vcc, v16, v238
	v_or_b32_e32 v16, 0xf1, v239
	s_nop 0
	v_cndmask_b32_e32 v107, v227, v91, vcc
	v_cmp_le_i32_e32 vcc, v16, v238
	v_or_b32_e32 v16, 0xd2, v239
	s_nop 0
	v_cndmask_b32_e32 v91, v227, v109, vcc
	v_cmp_le_i32_e32 vcc, v16, v238
	v_or_b32_e32 v16, 0xf2, v239
	s_nop 0
	v_cndmask_b32_e32 v108, v227, v92, vcc
	v_cmp_le_i32_e32 vcc, v16, v238
	v_or_b32_e32 v16, 0xd3, v239
	s_nop 0
	v_cndmask_b32_e32 v92, v227, v110, vcc
	v_cmp_le_i32_e32 vcc, v16, v238
	v_or_b32_e32 v16, 0xf3, v239
	s_nop 0
	v_cndmask_b32_e32 v109, v227, v93, vcc
	v_cmp_le_i32_e32 vcc, v16, v238
	v_or_b32_e32 v16, 0xd8, v239
	s_nop 0
	v_cndmask_b32_e32 v93, v227, v111, vcc
	v_cmp_le_i32_e32 vcc, v16, v238
	v_or_b32_e32 v16, 0xf8, v239
	s_nop 0
	v_cndmask_b32_e32 v110, v227, v94, vcc
	v_cmp_le_i32_e32 vcc, v16, v238
	v_or_b32_e32 v16, 0xd9, v239
	s_nop 0
	v_cndmask_b32_e32 v94, v227, v112, vcc
	v_cmp_le_i32_e32 vcc, v16, v238
	v_or_b32_e32 v16, 0xf9, v239
	s_nop 0
	v_cndmask_b32_e32 v111, v227, v95, vcc
	v_cmp_le_i32_e32 vcc, v16, v238
	v_or_b32_e32 v16, 0xda, v239
	s_nop 0
	v_cndmask_b32_e32 v95, v227, v113, vcc
	v_cmp_le_i32_e32 vcc, v16, v238
	v_or_b32_e32 v16, 0xfa, v239
	s_nop 0
	v_cndmask_b32_e32 v112, v227, v96, vcc
	v_cmp_le_i32_e32 vcc, v16, v238
	v_or_b32_e32 v16, 0xdb, v239
	s_nop 0
	v_cndmask_b32_e32 v96, v227, v114, vcc
	v_cmp_le_i32_e32 vcc, v16, v238
	v_sub_u32_e32 v16, v238, v239
	v_lshl_add_u32 v145, v16, 2, s40
	v_cndmask_b32_e32 v113, v227, v97, vcc
	v_or_b32_e32 v97, 0xfb, v239
	v_cmp_le_i32_e32 vcc, v97, v238
	ds_read2_b32 v[16:17], v145 offset0:63 offset1:64
	ds_read2_b32 v[84:85], v145 offset0:31 offset1:32
	v_cndmask_b32_e32 v97, v227, v115, vcc
	ds_read2_b32 v[114:115], v145 offset0:61 offset1:62
	ds_read2_b32 v[128:129], v145 offset0:29 offset1:30
	s_waitcnt lgkmcnt(3)
	v_add_f32_e32 v98, v82, v17
	s_waitcnt lgkmcnt(2)
	v_add_f32_e32 v82, v99, v85
	v_add_f32_e32 v99, v83, v16
	v_add_f32_e32 v83, v100, v84
	s_waitcnt lgkmcnt(1)
	v_add_f32_e32 v100, v101, v115
	s_waitcnt lgkmcnt(0)
	v_add_f32_e32 v84, v142, v129
	v_add_f32_e32 v101, v143, v114
	v_add_f32_e32 v85, v144, v128
	s_nop 0
	ds_read2_b32 v[16:17], v145 offset0:55 offset1:56
	ds_read2_b32 v[114:115], v145 offset0:23 offset1:24
	ds_read2_b32 v[128:129], v145 offset0:53 offset1:54
	ds_read2_b32 v[142:143], v145 offset0:21 offset1:22
	s_waitcnt lgkmcnt(3)
	v_add_f32_e32 v102, v102, v17
	s_waitcnt lgkmcnt(2)
	v_add_f32_e32 v86, v86, v115
	v_add_f32_e32 v103, v103, v16
	v_add_f32_e32 v87, v87, v114
	s_waitcnt lgkmcnt(1)
	v_add_f32_e32 v104, v104, v129
	s_waitcnt lgkmcnt(0)
	v_add_f32_e32 v88, v88, v143
	v_add_f32_e32 v105, v105, v128
	v_add_f32_e32 v89, v89, v142
	s_nop 0
	ds_read2_b32 v[16:17], v145 offset0:47 offset1:48
	ds_read2_b32 v[114:115], v145 offset0:15 offset1:16
	ds_read2_b32 v[128:129], v145 offset0:45 offset1:46
	ds_read2_b32 v[142:143], v145 offset0:13 offset1:14
	s_waitcnt lgkmcnt(3)
	v_add_f32_e32 v106, v106, v17
	s_waitcnt lgkmcnt(2)
	v_add_f32_e32 v90, v90, v115
	v_add_f32_e32 v107, v107, v16
	v_add_f32_e32 v91, v91, v114
	s_waitcnt lgkmcnt(1)
	v_add_f32_e32 v108, v108, v129
	s_waitcnt lgkmcnt(0)
	v_add_f32_e32 v92, v92, v143
	v_add_f32_e32 v109, v109, v128
	v_add_f32_e32 v93, v93, v142
	s_nop 0
	ds_read2_b32 v[16:17], v145 offset0:39 offset1:40
	ds_read2_b32 v[114:115], v145 offset0:7 offset1:8
	ds_read2_b32 v[128:129], v145 offset0:37 offset1:38
	ds_read2_b32 v[142:143], v145 offset0:5 offset1:6
	s_waitcnt lgkmcnt(3)
	v_add_f32_e32 v110, v110, v17
	s_waitcnt lgkmcnt(2)
	v_add_f32_e32 v94, v94, v115
	v_add_f32_e32 v111, v111, v16
	v_add_f32_e32 v95, v95, v114
	s_waitcnt lgkmcnt(1)
	v_add_f32_e32 v112, v112, v129
	s_waitcnt lgkmcnt(0)
	v_add_f32_e32 v96, v96, v143
	v_add_f32_e32 v113, v113, v128
	v_add_f32_e32 v97, v97, v142
	s_nop 0
	s_nop 0
	v_max_f32_e32 v16, v99, v98
	v_max3_f32 v17, v100, v101, v83
	v_max3_f32 v16, v16, v82, v84
	v_max3_f32 v16, v16, v85, v102
	v_max3_f32 v17, v17, v104, v105
	v_max3_f32 v16, v16, v103, v86
	v_max3_f32 v17, v17, v88, v89
	v_max3_f32 v16, v16, v87, v106
	v_max3_f32 v17, v17, v108, v109
	v_max3_f32 v16, v16, v107, v90
	v_max3_f32 v17, v17, v92, v93
	v_max3_f32 v16, v16, v91, v110
	v_max3_f32 v17, v17, v112, v113
	v_max3_f32 v16, v16, v111, v94
	v_max3_f32 v17, v17, v96, v97
	v_max3_f32 v16, v16, v95, v17
	v_mov_b32_e32 v17, v16
	s_nop 1
	v_permlane32_swap_b32_e32 v16, v17
	v_max_f32_e32 v16, v16, v17
	v_cmp_lt_f32_e32 vcc, s79, v16
	s_cmp_lg_u64 vcc, 0
	s_cselect_b64 s[0:1], -1, 0
	s_cbranch_vccnz .LBB0_346

.Lfin_join_l0:
	s_and_saveexec_b64 s[0:1], vcc
	v_add_f32_e32 v2, v2, v8
	ds_write_b32 v235, v2 offset:128
	s_or_b64 exec, exec, s[0:1]
	s_waitcnt lgkmcnt(0)
	ds_read_b128 v[4:7], v234 offset:128
	ds_read_b128 v[8:11], v234 offset:160
	s_lshl_b32 s0, s84, 8
	s_add_u32 s2, s6, s0
	s_addc_u32 s3, s7, 0
	s_waitcnt lgkmcnt(1)
	v_rcp_f32_e32 v14, v4
	v_rcp_f32_e32 v15, v5
	v_rcp_f32_e32 v16, v6
	v_rcp_f32_e32 v17, v7
	ds_read_b128 v[4:7], v234 offset:192
	s_lshl_b64 s[0:1], s[34:35], 11
	s_add_u32 s0, s2, s0
	s_addc_u32 s1, s3, s1
	s_lshl_b32 s2, s83, 12
	s_add_i32 s2, s2, 0
	v_lshlrev_b32_e32 v2, 1, v232
	s_add_i32 s2, s2, 0x16800
	v_and_b32_e32 v2, 0x70, v2
	s_waitcnt lgkmcnt(1)
	v_rcp_f32_e32 v82, v8
	v_rcp_f32_e32 v83, v9
	v_rcp_f32_e32 v84, v10
	v_rcp_f32_e32 v85, v11
	ds_read_b128 v[8:11], v234 offset:224
	s_waitcnt lgkmcnt(1)
	v_rcp_f32_e32 v86, v4
	v_lshlrev_b32_e32 v4, 1, v231
	v_add_u32_e32 v95, s2, v2
	v_lshl_add_u64 v[12:13], s[0:1], 0, v[2:3]
	v_lshlrev_b32_e32 v2, 9, v229
	v_add3_u32 v97, s2, v4, v2
	v_mul_f32_e32 v2, v66, v14
	v_cvt_pk_bf16_f32 v2, v2, s0
	ds_write_b16 v97, v2
	v_mul_f32_e32 v2, v50, v14
	v_cvt_pk_bf16_f32 v2, v2, s0
	ds_write_b16 v97, v2 offset:64
	v_mul_f32_e32 v2, v67, v15
	v_cvt_pk_bf16_f32 v2, v2, s0
	ds_write_b16 v97, v2 offset:128
	v_mul_f32_e32 v2, v51, v15
	v_cvt_pk_bf16_f32 v2, v2, s0
	ds_write_b16 v97, v2 offset:192
	v_mul_f32_e32 v2, v68, v16
	v_cvt_pk_bf16_f32 v2, v2, s0
	ds_write_b16 v97, v2 offset:256
	v_mul_f32_e32 v2, v52, v16
	v_cvt_pk_bf16_f32 v2, v2, s0
	ds_write_b16 v97, v2 offset:320
	v_mul_f32_e32 v2, v69, v17
	v_cvt_pk_bf16_f32 v2, v2, s0
	ds_write_b16 v97, v2 offset:384
	v_mul_f32_e32 v2, v53, v17
	v_cvt_pk_bf16_f32 v2, v2, s0
	ds_write_b16 v97, v2 offset:448
	v_mul_f32_e32 v2, v70, v82
	v_cvt_pk_bf16_f32 v2, v2, s0
	ds_write_b16 v97, v2 offset:1024
	v_mul_f32_e32 v2, v54, v82
	v_cvt_pk_bf16_f32 v2, v2, s0
	ds_write_b16 v97, v2 offset:1088
	v_mul_f32_e32 v2, v71, v83
	v_cvt_pk_bf16_f32 v2, v2, s0
	ds_write_b16 v97, v2 offset:1152
	v_mul_f32_e32 v2, v55, v83
	v_cvt_pk_bf16_f32 v2, v2, s0
	ds_write_b16 v97, v2 offset:1216
	v_mul_f32_e32 v2, v72, v84
	v_cvt_pk_bf16_f32 v2, v2, s0
	ds_write_b16 v97, v2 offset:1280
	v_mul_f32_e32 v2, v56, v84
	v_cvt_pk_bf16_f32 v2, v2, s0
	ds_write_b16 v97, v2 offset:1344
	v_mul_f32_e32 v2, v73, v85
	v_cvt_pk_bf16_f32 v2, v2, s0
	ds_write_b16 v97, v2 offset:1408
	v_mul_f32_e32 v2, v57, v85
	v_cvt_pk_bf16_f32 v2, v2, s0
	v_rcp_f32_e32 v87, v5
	ds_write_b16 v97, v2 offset:1472
	v_mul_f32_e32 v2, v74, v86
	v_cvt_pk_bf16_f32 v2, v2, s0
	ds_write_b16 v97, v2 offset:2048
	v_mul_f32_e32 v2, v58, v86
	v_cvt_pk_bf16_f32 v2, v2, s0
	v_rcp_f32_e32 v88, v6
	ds_write_b16 v97, v2 offset:2112
	v_mul_f32_e32 v2, v75, v87
	v_cvt_pk_bf16_f32 v2, v2, s0
	ds_write_b16 v97, v2 offset:2176
	v_mul_f32_e32 v2, v59, v87
	v_cvt_pk_bf16_f32 v2, v2, s0
	v_rcp_f32_e32 v89, v7
	ds_write_b16 v97, v2 offset:2240
	v_mul_f32_e32 v2, v76, v88
	v_cvt_pk_bf16_f32 v2, v2, s0
	ds_write_b16 v97, v2 offset:2304
	v_mul_f32_e32 v2, v60, v88
	v_cvt_pk_bf16_f32 v2, v2, s0
	s_waitcnt lgkmcnt(14)
	v_rcp_f32_e32 v90, v8
	ds_write_b16 v97, v2 offset:2368
	v_mul_f32_e32 v2, v77, v89
	v_cvt_pk_bf16_f32 v2, v2, s0
	ds_write_b16 v97, v2 offset:2432
	v_mul_f32_e32 v2, v61, v89
	v_cvt_pk_bf16_f32 v2, v2, s0
	v_rcp_f32_e32 v91, v9
	ds_write_b16 v97, v2 offset:2496
	v_mul_f32_e32 v2, v78, v90
	v_cvt_pk_bf16_f32 v2, v2, s0
	ds_write_b16 v97, v2 offset:3072
	v_mul_f32_e32 v2, v62, v90
	v_cvt_pk_bf16_f32 v2, v2, s0
	v_rcp_f32_e32 v92, v10
	ds_write_b16 v97, v2 offset:3136
	v_mul_f32_e32 v2, v79, v91
	v_cvt_pk_bf16_f32 v2, v2, s0
	ds_write_b16 v97, v2 offset:3200
	v_mul_f32_e32 v2, v63, v91
	v_cvt_pk_bf16_f32 v2, v2, s0
	v_rcp_f32_e32 v93, v11
	ds_write_b16 v97, v2 offset:3264
	v_mul_f32_e32 v2, v80, v92
	v_cvt_pk_bf16_f32 v2, v2, s0
	ds_write_b16 v97, v2 offset:3328
	v_mul_f32_e32 v2, v64, v92
	v_cvt_pk_bf16_f32 v2, v2, s0
	ds_write_b16 v97, v2 offset:3392
	v_mul_f32_e32 v2, v81, v93
	v_cvt_pk_bf16_f32 v2, v2, s0
	ds_write_b16 v97, v2 offset:3456
	v_mul_f32_e32 v2, v65, v93
	v_lshrrev_b32_e32 v94, 3, v230
	v_cvt_pk_bf16_f32 v2, v2, s0
	ds_write_b16 v97, v2 offset:3520
	v_or_b32_e32 v52, 8, v94
	v_lshl_add_u32 v96, v94, 7, v95
	s_waitcnt lgkmcnt(0)
	v_lshl_add_u32 v58, v52, 7, v95
	ds_read_b128 v[4:7], v96
	ds_read_b128 v[8:11], v58
	v_lshlrev_b32_e32 v2, 11, v94
	v_lshl_add_u64 v[50:51], v[12:13], 0, v[2:3]
	v_lshlrev_b32_e32 v2, 11, v52
	v_lshl_add_u64 v[52:53], v[12:13], 0, v[2:3]
	v_or_b32_e32 v2, 16, v94
	v_or_b32_e32 v56, 24, v94
	v_lshl_add_u32 v59, v2, 7, v95
	v_lshl_add_u32 v60, v56, 7, v95
	s_waitcnt lgkmcnt(1)
	global_store_dwordx4 v[50:51], v[4:7], off
	ds_read_b128 v[4:7], v59
	s_waitcnt lgkmcnt(1)
	global_store_dwordx4 v[52:53], v[8:11], off
	ds_read_b128 v[8:11], v60
	v_lshlrev_b32_e32 v2, 11, v2
	v_lshl_add_u64 v[54:55], v[12:13], 0, v[2:3]
	v_lshlrev_b32_e32 v2, 11, v56
	v_lshl_add_u64 v[56:57], v[12:13], 0, v[2:3]
	v_mul_f32_e32 v2, v34, v14
	s_waitcnt lgkmcnt(1)
	global_store_dwordx4 v[54:55], v[4:7], off
	s_waitcnt lgkmcnt(0)
	global_store_dwordx4 v[56:57], v[8:11], off
	v_cvt_pk_bf16_f32 v2, v2, s0
	s_waitcnt lgkmcnt(0)
	ds_write_b16 v97, v2
	v_mul_f32_e32 v2, v18, v14
	v_cvt_pk_bf16_f32 v2, v2, s0
	ds_write_b16 v97, v2 offset:64
	v_mul_f32_e32 v2, v35, v15
	v_cvt_pk_bf16_f32 v2, v2, s0
	ds_write_b16 v97, v2 offset:128
	v_mul_f32_e32 v2, v19, v15
	v_cvt_pk_bf16_f32 v2, v2, s0
	ds_write_b16 v97, v2 offset:192
	v_mul_f32_e32 v2, v36, v16
	v_cvt_pk_bf16_f32 v2, v2, s0
	ds_write_b16 v97, v2 offset:256
	v_mul_f32_e32 v2, v20, v16
	v_cvt_pk_bf16_f32 v2, v2, s0
	ds_write_b16 v97, v2 offset:320
	v_mul_f32_e32 v2, v37, v17
	v_cvt_pk_bf16_f32 v2, v2, s0
	ds_write_b16 v97, v2 offset:384
	v_mul_f32_e32 v2, v21, v17
	v_cvt_pk_bf16_f32 v2, v2, s0
	ds_write_b16 v97, v2 offset:448
	v_mul_f32_e32 v2, v38, v82
	v_cvt_pk_bf16_f32 v2, v2, s0
	ds_write_b16 v97, v2 offset:1024
	v_mul_f32_e32 v2, v22, v82
	v_cvt_pk_bf16_f32 v2, v2, s0
	ds_write_b16 v97, v2 offset:1088
	v_mul_f32_e32 v2, v39, v83
	v_cvt_pk_bf16_f32 v2, v2, s0
	ds_write_b16 v97, v2 offset:1152
	v_mul_f32_e32 v2, v23, v83
	v_cvt_pk_bf16_f32 v2, v2, s0
	ds_write_b16 v97, v2 offset:1216
	v_mul_f32_e32 v2, v40, v84
	v_cvt_pk_bf16_f32 v2, v2, s0
	ds_write_b16 v97, v2 offset:1280
	v_mul_f32_e32 v2, v24, v84
	v_cvt_pk_bf16_f32 v2, v2, s0
	ds_write_b16 v97, v2 offset:1344
	v_mul_f32_e32 v2, v41, v85
	v_cvt_pk_bf16_f32 v2, v2, s0
	ds_write_b16 v97, v2 offset:1408
	v_mul_f32_e32 v2, v25, v85
	v_cvt_pk_bf16_f32 v2, v2, s0
	ds_write_b16 v97, v2 offset:1472
	v_mul_f32_e32 v2, v42, v86
	v_cvt_pk_bf16_f32 v2, v2, s0
	ds_write_b16 v97, v2 offset:2048
	v_mul_f32_e32 v2, v26, v86
	v_cvt_pk_bf16_f32 v2, v2, s0
	ds_write_b16 v97, v2 offset:2112
	v_mul_f32_e32 v2, v43, v87
	v_cvt_pk_bf16_f32 v2, v2, s0
	ds_write_b16 v97, v2 offset:2176
	v_mul_f32_e32 v2, v27, v87
	v_cvt_pk_bf16_f32 v2, v2, s0
	ds_write_b16 v97, v2 offset:2240
	v_mul_f32_e32 v2, v44, v88
	v_cvt_pk_bf16_f32 v2, v2, s0
	ds_write_b16 v97, v2 offset:2304
	v_mul_f32_e32 v2, v28, v88
	v_cvt_pk_bf16_f32 v2, v2, s0
	ds_write_b16 v97, v2 offset:2368
	v_mul_f32_e32 v2, v45, v89
	v_cvt_pk_bf16_f32 v2, v2, s0
	ds_write_b16 v97, v2 offset:2432
	v_mul_f32_e32 v2, v29, v89
	v_cvt_pk_bf16_f32 v2, v2, s0
	ds_write_b16 v97, v2 offset:2496
	v_mul_f32_e32 v2, v46, v90
	v_cvt_pk_bf16_f32 v2, v2, s0
	ds_write_b16 v97, v2 offset:3072
	v_mul_f32_e32 v2, v30, v90
	v_cvt_pk_bf16_f32 v2, v2, s0
	ds_write_b16 v97, v2 offset:3136
	v_mul_f32_e32 v2, v47, v91
	v_cvt_pk_bf16_f32 v2, v2, s0
	ds_write_b16 v97, v2 offset:3200
	v_mul_f32_e32 v2, v31, v91
	v_cvt_pk_bf16_f32 v2, v2, s0
	ds_write_b16 v97, v2 offset:3264
	v_mul_f32_e32 v2, v48, v92
	v_cvt_pk_bf16_f32 v2, v2, s0
	ds_write_b16 v97, v2 offset:3328
	v_mul_f32_e32 v2, v32, v92
	v_cvt_pk_bf16_f32 v2, v2, s0
	ds_write_b16 v97, v2 offset:3392
	v_mul_f32_e32 v2, v49, v93
	v_cvt_pk_bf16_f32 v2, v2, s0
	ds_write_b16 v97, v2 offset:3456
	v_mul_f32_e32 v2, v33, v93
	v_cvt_pk_bf16_f32 v2, v2, s0
	ds_write_b16 v97, v2 offset:3520
	s_waitcnt lgkmcnt(0)
	ds_read_b128 v[4:7], v96
	ds_read_b128 v[8:11], v58
	ds_read_b128 v[12:15], v59
	ds_read_b128 v[16:19], v60
	s_waitcnt lgkmcnt(3)
	global_store_dwordx4 v[50:51], v[4:7], off offset:128
	s_waitcnt lgkmcnt(2)
	global_store_dwordx4 v[52:53], v[8:11], off offset:128
	s_waitcnt lgkmcnt(1)
	global_store_dwordx4 v[54:55], v[12:15], off offset:128
	s_waitcnt lgkmcnt(0)
	global_store_dwordx4 v[56:57], v[16:19], off offset:128
	s_waitcnt lgkmcnt(0)
	s_waitcnt lgkmcnt(0)
	s_barrier
	s_cmp_lt_u32 s21, 2
	s_cbranch_scc1 .LBB0_259
	v_mov_b32_e32 v6, v0
	s_lshl_b32 s0, s82, 8
	v_ashrrev_i32_e32 v4, 1, v6
	s_or_b32 s0, s8, s0
	s_mov_b32 s1, s9
	v_ashrrev_i32_e32 v5, 31, v4
	v_lshl_add_u64 v[12:13], s[0:1], 0, v[4:5]
	v_lshlrev_b32_e32 v2, 6, v6
	v_lshlrev_b64 v[4:5], 11, v[12:13]
	v_and_b32_e32 v7, 64, v2
	v_lshl_add_u64 v[4:5], s[6:7], 0, v[4:5]
	v_lshlrev_b32_e32 v2, 1, v7
	v_lshl_add_u64 v[4:5], v[4:5], 0, v[2:3]
	s_waitcnt vmcnt(0)
	s_barrier
	global_load_dwordx2 v[16:17], v[4:5], off sc1
	global_load_dwordx2 v[18:19], v[4:5], off offset:256 sc1
	global_load_dwordx2 v[24:25], v[4:5], off offset:8 sc1
	global_load_dwordx2 v[26:27], v[4:5], off offset:264 sc1
	global_load_dwordx2 v[30:31], v[4:5], off offset:16 sc1
	global_load_dwordx2 v[34:35], v[4:5], off offset:272 sc1
	global_load_dwordx2 v[42:43], v[4:5], off offset:24 sc1
	global_load_dwordx2 v[50:51], v[4:5], off offset:280 sc1
	v_lshlrev_b32_e32 v6, 2, v6
	v_bitop3_b32 v83, v6, 4, v228 bitop3:0x6c
	v_lshlrev_b32_e32 v82, 2, v7
	global_load_dwordx2 v[54:55], v[4:5], off offset:32 sc1
	global_load_dwordx2 v[60:61], v[4:5], off offset:288 sc1
	global_load_dwordx2 v[74:75], v[4:5], off offset:40 sc1
	global_load_dwordx2 v[84:85], v[4:5], off offset:296 sc1
	global_load_dwordx2 v[86:87], v[4:5], off offset:48 sc1
	global_load_dwordx2 v[88:89], v[4:5], off offset:304 sc1
	global_load_dwordx2 v[90:91], v[4:5], off offset:56 sc1
	global_load_dwordx2 v[28:29], v[4:5], off offset:312 sc1
	global_load_dwordx2 v[58:59], v[4:5], off offset:64 sc1
	global_load_dwordx2 v[36:37], v[4:5], off offset:320 sc1
	global_load_dwordx2 v[66:67], v[4:5], off offset:72 sc1
	global_load_dwordx2 v[44:45], v[4:5], off offset:328 sc1
	global_load_dwordx2 v[62:63], v[4:5], off offset:80 sc1
	global_load_dwordx2 v[52:53], v[4:5], off offset:336 sc1
	global_load_dwordx2 v[76:77], v[4:5], off offset:88 sc1
	global_load_dwordx2 v[32:33], v[4:5], off offset:344 sc1
	global_load_dwordx2 v[68:69], v[4:5], off offset:96 sc1
	global_load_dwordx2 v[38:39], v[4:5], off offset:352 sc1
	global_load_dwordx2 v[80:81], v[4:5], off offset:104 sc1
	global_load_dwordx2 v[20:21], v[4:5], off offset:360 sc1
	global_load_dwordx2 v[46:47], v[4:5], off offset:112 sc1
	global_load_dwordx2 v[22:23], v[4:5], off offset:368 sc1
	global_load_dwordx2 v[56:57], v[4:5], off offset:120 sc1
	global_load_dwordx2 v[48:49], v[4:5], off offset:376 sc1
	s_nop 0
	global_load_dwordx4 v[4:7], v82, s[58:59] offset:16
	global_load_dwordx4 v[8:11], v82, s[58:59]
	v_mov_b64_e32 v[14:15], s[24:25]
	v_mad_u64_u32 v[14:15], s[0:1], v12, s5, v[14:15]
	v_mad_i32_i24 v15, v13, s5, v15
	v_lshl_add_u64 v[12:13], v[14:15], 0, v[2:3]
	s_mov_b32 s0, 0xf800000
	s_waitcnt vmcnt(33)
	v_lshlrev_b32_e32 v41, 16, v17
	v_lshlrev_b32_e32 v40, 16, v16
	s_waitcnt vmcnt(32)
	v_lshlrev_b32_e32 v65, 16, v19
	v_lshlrev_b32_e32 v64, 16, v18
	v_and_b32_e32 v17, 0xffff0000, v17
	v_and_b32_e32 v16, 0xffff0000, v16
	v_and_b32_e32 v19, 0xffff0000, v19
	v_and_b32_e32 v18, 0xffff0000, v18
	s_waitcnt vmcnt(29)
	v_lshlrev_b32_e32 v95, 16, v31
	v_lshlrev_b32_e32 v94, 16, v30
	s_waitcnt vmcnt(28)
	v_lshlrev_b32_e32 v97, 16, v35
	v_lshlrev_b32_e32 v96, 16, v34
	v_and_b32_e32 v31, 0xffff0000, v31
	v_and_b32_e32 v30, 0xffff0000, v30
	v_and_b32_e32 v35, 0xffff0000, v35
	v_and_b32_e32 v34, 0xffff0000, v34
	v_pk_fma_f32 v[72:73], v[214:215], v[18:19], v[16:17] neg_lo:[1,0,0] neg_hi:[1,0,0]
	v_pk_fma_f32 v[18:19], v[214:215], v[96:97], v[94:95] neg_lo:[1,0,0] neg_hi:[1,0,0]
	v_pk_fma_f32 v[16:17], v[214:215], v[34:35], v[30:31] neg_lo:[1,0,0] neg_hi:[1,0,0]
	v_lshlrev_b32_e32 v71, 16, v25
	v_lshlrev_b32_e32 v70, 16, v24
	v_lshlrev_b32_e32 v93, 16, v27
	v_lshlrev_b32_e32 v92, 16, v26
	v_and_b32_e32 v25, 0xffff0000, v25
	v_and_b32_e32 v24, 0xffff0000, v24
	v_and_b32_e32 v27, 0xffff0000, v27
	v_and_b32_e32 v26, 0xffff0000, v26
	v_mov_b32_e32 v30, v18
	v_mov_b32_e32 v31, v16
	v_mul_f32_e32 v34, v16, v16
	v_pk_fma_f32 v[78:79], v[214:215], v[64:65], v[40:41] neg_lo:[1,0,0] neg_hi:[1,0,0]
	v_pk_fma_f32 v[64:65], v[214:215], v[26:27], v[24:25] neg_lo:[1,0,0] neg_hi:[1,0,0]
	v_pk_fma_f32 v[30:31], v[30:31], v[30:31], v[34:35] op_sel_hi:[1,1,0]
	v_mov_b32_e32 v34, v19
	v_mov_b32_e32 v35, v17
	v_mul_f32_e32 v40, v17, v17
	v_pk_fma_f32 v[70:71], v[214:215], v[92:93], v[70:71] neg_lo:[1,0,0] neg_hi:[1,0,0]
	v_pk_mul_f32 v[24:25], v[72:73], v[72:73]
	v_pk_mul_f32 v[26:27], v[64:65], v[64:65]
	v_pk_fma_f32 v[34:35], v[34:35], v[34:35], v[40:41] op_sel_hi:[1,1,0]
	s_waitcnt vmcnt(27)
	v_lshlrev_b32_e32 v41, 16, v43
	v_lshlrev_b32_e32 v40, 16, v42
	s_waitcnt vmcnt(26)
	v_lshlrev_b32_e32 v93, 16, v51
	v_lshlrev_b32_e32 v92, 16, v50
	v_and_b32_e32 v43, 0xffff0000, v43
	v_and_b32_e32 v42, 0xffff0000, v42
	v_and_b32_e32 v51, 0xffff0000, v51
	v_and_b32_e32 v50, 0xffff0000, v50
	v_pk_fma_f32 v[24:25], v[78:79], v[78:79], v[24:25]
	v_pk_fma_f32 v[26:27], v[70:71], v[70:71], v[26:27]
	v_pk_fma_f32 v[40:41], v[214:215], v[92:93], v[40:41] neg_lo:[1,0,0] neg_hi:[1,0,0]
	v_pk_fma_f32 v[50:51], v[214:215], v[50:51], v[42:43] neg_lo:[1,0,0] neg_hi:[1,0,0]
	v_pk_add_f32 v[24:25], v[24:25], v[24:25] op_sel:[0,1] op_sel_hi:[1,0]
	v_pk_add_f32 v[26:27], v[26:27], v[26:27] op_sel:[0,1] op_sel_hi:[1,0]
	v_pk_mul_f32 v[42:43], v[40:41], v[40:41]
	v_pk_mul_f32 v[92:93], v[50:51], v[50:51]
	v_mov_b32_e32 v25, v42
	v_mov_b32_e32 v27, v92
	v_mov_b32_e32 v31, v43
	v_mov_b32_e32 v35, v93
	v_pk_add_f32 v[24:25], v[24:25], v[26:27]
	v_pk_add_f32 v[26:27], v[30:31], v[34:35]
	s_waitcnt vmcnt(24)
	v_and_b32_e32 v31, 0xffff0000, v61
	v_pk_add_f32 v[24:25], v[24:25], v[26:27]
	v_lshlrev_b32_e32 v27, 16, v61
	v_pk_add_f32 v[92:93], v[24:25], v[24:25] op_sel:[0,1] op_sel_hi:[1,0]
	v_lshlrev_b32_e32 v25, 16, v55
	v_lshlrev_b32_e32 v24, 16, v54
	v_lshlrev_b32_e32 v26, 16, v60
	v_pk_fma_f32 v[26:27], v[214:215], v[26:27], v[24:25] neg_lo:[1,0,0] neg_hi:[1,0,0]
	v_and_b32_e32 v25, 0xffff0000, v55
	v_and_b32_e32 v24, 0xffff0000, v54
	v_and_b32_e32 v30, 0xffff0000, v60
	v_pk_fma_f32 v[34:35], v[214:215], v[30:31], v[24:25] neg_lo:[1,0,0] neg_hi:[1,0,0]
	s_waitcnt vmcnt(22)
	v_lshlrev_b32_e32 v31, 16, v85
	v_pk_mul_f32 v[24:25], v[34:35], v[34:35]
	v_lshlrev_b32_e32 v30, 16, v84
	v_pk_fma_f32 v[24:25], v[26:27], v[26:27], v[24:25]
	s_waitcnt vmcnt(0)
	v_mov_b32_e32 v15, v10
	v_pk_add_f32 v[60:61], v[24:25], v[24:25] op_sel:[0,1] op_sel_hi:[1,0]
	v_lshlrev_b32_e32 v25, 16, v75
	v_lshlrev_b32_e32 v24, 16, v74
	v_pk_fma_f32 v[42:43], v[214:215], v[30:31], v[24:25] neg_lo:[1,0,0] neg_hi:[1,0,0]
	v_and_b32_e32 v25, 0xffff0000, v75
	v_and_b32_e32 v24, 0xffff0000, v74
	v_and_b32_e32 v31, 0xffff0000, v85
	v_and_b32_e32 v30, 0xffff0000, v84
	v_pk_fma_f32 v[54:55], v[214:215], v[30:31], v[24:25] neg_lo:[1,0,0] neg_hi:[1,0,0]
	v_mov_b32_e32 v24, v42
	v_mov_b32_e32 v25, v54
	v_mul_f32_e32 v30, v54, v54
	v_pk_fma_f32 v[74:75], v[24:25], v[24:25], v[30:31] op_sel_hi:[1,1,0]
	v_mov_b32_e32 v24, v43
	v_mov_b32_e32 v25, v55
	v_mul_f32_e32 v30, v55, v55
	v_pk_fma_f32 v[84:85], v[24:25], v[24:25], v[30:31] op_sel_hi:[1,1,0]
	v_lshlrev_b32_e32 v25, 16, v87
	v_lshlrev_b32_e32 v24, 16, v86
	v_lshlrev_b32_e32 v31, 16, v89
	v_lshlrev_b32_e32 v30, 16, v88
	v_pk_fma_f32 v[24:25], v[214:215], v[30:31], v[24:25] neg_lo:[1,0,0] neg_hi:[1,0,0]
	v_and_b32_e32 v31, 0xffff0000, v87
	v_and_b32_e32 v30, 0xffff0000, v86
	v_and_b32_e32 v87, 0xffff0000, v89
	v_and_b32_e32 v86, 0xffff0000, v88
	v_pk_fma_f32 v[30:31], v[214:215], v[86:87], v[30:31] neg_lo:[1,0,0] neg_hi:[1,0,0]
	v_pk_mul_f32 v[86:87], v[24:25], v[24:25]
	v_pk_mul_f32 v[88:89], v[30:31], v[30:31]
	v_mov_b32_e32 v93, v86
	v_mov_b32_e32 v61, v88
	v_mov_b32_e32 v75, v87
	v_mov_b32_e32 v85, v89
	v_pk_add_f32 v[60:61], v[92:93], v[60:61]
	v_pk_add_f32 v[74:75], v[74:75], v[84:85]
	v_lshlrev_b32_e32 v89, 16, v37
	v_pk_add_f32 v[60:61], v[60:61], v[74:75]
	v_lshlrev_b32_e32 v75, 16, v29
	v_pk_add_f32 v[84:85], v[60:61], v[60:61] op_sel:[0,1] op_sel_hi:[1,0]
	v_lshlrev_b32_e32 v61, 16, v91
	v_lshlrev_b32_e32 v60, 16, v90
	v_lshlrev_b32_e32 v74, 16, v28
	v_pk_fma_f32 v[60:61], v[214:215], v[74:75], v[60:61] neg_lo:[1,0,0] neg_hi:[1,0,0]
	v_and_b32_e32 v75, 0xffff0000, v91
	v_and_b32_e32 v74, 0xffff0000, v90
	v_and_b32_e32 v29, 0xffff0000, v29
	v_and_b32_e32 v28, 0xffff0000, v28
	v_pk_fma_f32 v[74:75], v[214:215], v[28:29], v[74:75] neg_lo:[1,0,0] neg_hi:[1,0,0]
	v_lshlrev_b32_e32 v88, 16, v36
	v_pk_mul_f32 v[28:29], v[74:75], v[74:75]
	v_and_b32_e32 v37, 0xffff0000, v37
	v_pk_fma_f32 v[28:29], v[60:61], v[60:61], v[28:29]
	v_and_b32_e32 v36, 0xffff0000, v36
	v_pk_add_f32 v[86:87], v[28:29], v[28:29] op_sel:[0,1] op_sel_hi:[1,0]
	v_lshlrev_b32_e32 v29, 16, v59
	v_lshlrev_b32_e32 v28, 16, v58
	v_and_b32_e32 v59, 0xffff0000, v59
	v_and_b32_e32 v58, 0xffff0000, v58
	v_pk_fma_f32 v[28:29], v[214:215], v[88:89], v[28:29] neg_lo:[1,0,0] neg_hi:[1,0,0]
	v_pk_fma_f32 v[36:37], v[214:215], v[36:37], v[58:59] neg_lo:[1,0,0] neg_hi:[1,0,0]
	v_mov_b32_e32 v58, v28
	v_mov_b32_e32 v59, v36
	v_mul_f32_e32 v88, v36, v36
	v_pk_fma_f32 v[88:89], v[58:59], v[58:59], v[88:89] op_sel_hi:[1,1,0]
	v_mov_b32_e32 v58, v29
	v_mov_b32_e32 v59, v37
	v_mul_f32_e32 v90, v37, v37
	v_pk_fma_f32 v[90:91], v[58:59], v[58:59], v[90:91] op_sel_hi:[1,1,0]
	v_lshlrev_b32_e32 v59, 16, v67
	v_lshlrev_b32_e32 v58, 16, v66
	v_lshlrev_b32_e32 v93, 16, v45
	v_lshlrev_b32_e32 v92, 16, v44
	v_and_b32_e32 v67, 0xffff0000, v67
	v_and_b32_e32 v66, 0xffff0000, v66
	v_and_b32_e32 v45, 0xffff0000, v45
	v_and_b32_e32 v44, 0xffff0000, v44
	v_pk_fma_f32 v[58:59], v[214:215], v[92:93], v[58:59] neg_lo:[1,0,0] neg_hi:[1,0,0]
	v_pk_fma_f32 v[66:67], v[214:215], v[44:45], v[66:67] neg_lo:[1,0,0] neg_hi:[1,0,0]
	v_pk_mul_f32 v[44:45], v[58:59], v[58:59]
	v_pk_mul_f32 v[92:93], v[66:67], v[66:67]
	v_mov_b32_e32 v85, v44
	v_mov_b32_e32 v87, v92
	v_mov_b32_e32 v89, v45
	v_mov_b32_e32 v91, v93
	v_pk_add_f32 v[84:85], v[84:85], v[86:87]
	v_pk_add_f32 v[44:45], v[88:89], v[90:91]
	v_lshlrev_b32_e32 v87, 16, v53
	v_pk_add_f32 v[44:45], v[84:85], v[44:45]
	v_lshlrev_b32_e32 v86, 16, v52
	v_pk_add_f32 v[84:85], v[44:45], v[44:45] op_sel:[0,1] op_sel_hi:[1,0]
	v_lshlrev_b32_e32 v45, 16, v63
	v_lshlrev_b32_e32 v44, 16, v62
	v_and_b32_e32 v63, 0xffff0000, v63
	v_and_b32_e32 v62, 0xffff0000, v62
	v_and_b32_e32 v53, 0xffff0000, v53
	v_and_b32_e32 v52, 0xffff0000, v52
	v_pk_fma_f32 v[52:53], v[214:215], v[52:53], v[62:63] neg_lo:[1,0,0] neg_hi:[1,0,0]
	v_pk_fma_f32 v[44:45], v[214:215], v[86:87], v[44:45] neg_lo:[1,0,0] neg_hi:[1,0,0]
	v_pk_mul_f32 v[62:63], v[52:53], v[52:53]
	v_lshlrev_b32_e32 v89, 16, v33
	v_pk_fma_f32 v[62:63], v[44:45], v[44:45], v[62:63]
	v_lshlrev_b32_e32 v88, 16, v32
	v_pk_add_f32 v[86:87], v[62:63], v[62:63] op_sel:[0,1] op_sel_hi:[1,0]
	v_lshlrev_b32_e32 v63, 16, v77
	v_lshlrev_b32_e32 v62, 16, v76
	v_and_b32_e32 v77, 0xffff0000, v77
	v_and_b32_e32 v76, 0xffff0000, v76
	v_and_b32_e32 v33, 0xffff0000, v33
	v_and_b32_e32 v32, 0xffff0000, v32
	v_pk_fma_f32 v[62:63], v[214:215], v[88:89], v[62:63] neg_lo:[1,0,0] neg_hi:[1,0,0]
	v_pk_fma_f32 v[76:77], v[214:215], v[32:33], v[76:77] neg_lo:[1,0,0] neg_hi:[1,0,0]
	v_mov_b32_e32 v32, v62
	v_mov_b32_e32 v33, v76
	v_mul_f32_e32 v88, v76, v76
	v_pk_fma_f32 v[88:89], v[32:33], v[32:33], v[88:89] op_sel_hi:[1,1,0]
	v_mov_b32_e32 v32, v63
	v_mov_b32_e32 v33, v77
	v_mul_f32_e32 v90, v77, v77
	v_pk_fma_f32 v[90:91], v[32:33], v[32:33], v[90:91] op_sel_hi:[1,1,0]
	v_lshlrev_b32_e32 v33, 16, v69
	v_lshlrev_b32_e32 v32, 16, v68
	v_lshlrev_b32_e32 v93, 16, v39
	v_lshlrev_b32_e32 v92, 16, v38
	v_and_b32_e32 v69, 0xffff0000, v69
	v_and_b32_e32 v68, 0xffff0000, v68
	v_and_b32_e32 v39, 0xffff0000, v39
	v_and_b32_e32 v38, 0xffff0000, v38
	v_pk_fma_f32 v[32:33], v[214:215], v[92:93], v[32:33] neg_lo:[1,0,0] neg_hi:[1,0,0]
	v_pk_fma_f32 v[38:39], v[214:215], v[38:39], v[68:69] neg_lo:[1,0,0] neg_hi:[1,0,0]
	v_pk_mul_f32 v[68:69], v[32:33], v[32:33]
	v_pk_mul_f32 v[92:93], v[38:39], v[38:39]
	v_mov_b32_e32 v85, v68
	v_mov_b32_e32 v87, v92
	v_mov_b32_e32 v89, v69
	v_mov_b32_e32 v91, v93
	v_pk_add_f32 v[84:85], v[84:85], v[86:87]
	v_pk_add_f32 v[68:69], v[88:89], v[90:91]
	v_lshlrev_b32_e32 v87, 16, v21
	v_pk_add_f32 v[68:69], v[84:85], v[68:69]
	v_lshlrev_b32_e32 v86, 16, v20
	v_pk_add_f32 v[84:85], v[68:69], v[68:69] op_sel:[0,1] op_sel_hi:[1,0]
	v_lshlrev_b32_e32 v69, 16, v81
	v_lshlrev_b32_e32 v68, 16, v80
	v_and_b32_e32 v81, 0xffff0000, v81
	v_and_b32_e32 v80, 0xffff0000, v80
	v_and_b32_e32 v21, 0xffff0000, v21
	v_and_b32_e32 v20, 0xffff0000, v20
	v_pk_fma_f32 v[80:81], v[214:215], v[20:21], v[80:81] neg_lo:[1,0,0] neg_hi:[1,0,0]
	v_pk_fma_f32 v[68:69], v[214:215], v[86:87], v[68:69] neg_lo:[1,0,0] neg_hi:[1,0,0]
	v_pk_mul_f32 v[20:21], v[80:81], v[80:81]
	v_lshlrev_b32_e32 v89, 16, v23
	v_pk_fma_f32 v[20:21], v[68:69], v[68:69], v[20:21]
	v_lshlrev_b32_e32 v88, 16, v22
	v_pk_add_f32 v[86:87], v[20:21], v[20:21] op_sel:[0,1] op_sel_hi:[1,0]
	v_lshlrev_b32_e32 v21, 16, v47
	v_lshlrev_b32_e32 v20, 16, v46
	v_and_b32_e32 v47, 0xffff0000, v47
	v_and_b32_e32 v46, 0xffff0000, v46
	v_and_b32_e32 v23, 0xffff0000, v23
	v_and_b32_e32 v22, 0xffff0000, v22
	v_pk_fma_f32 v[20:21], v[214:215], v[88:89], v[20:21] neg_lo:[1,0,0] neg_hi:[1,0,0]
	v_pk_fma_f32 v[22:23], v[214:215], v[22:23], v[46:47] neg_lo:[1,0,0] neg_hi:[1,0,0]
	v_mov_b32_e32 v46, v20
	v_mov_b32_e32 v47, v22
	v_mul_f32_e32 v88, v22, v22
	v_pk_fma_f32 v[88:89], v[46:47], v[46:47], v[88:89] op_sel_hi:[1,1,0]
	v_mov_b32_e32 v46, v21
	v_mov_b32_e32 v47, v23
	v_mul_f32_e32 v90, v23, v23
	v_pk_fma_f32 v[90:91], v[46:47], v[46:47], v[90:91] op_sel_hi:[1,1,0]
	v_lshlrev_b32_e32 v47, 16, v57
	v_lshlrev_b32_e32 v46, 16, v56
	v_lshlrev_b32_e32 v93, 16, v49
	v_lshlrev_b32_e32 v92, 16, v48
	v_and_b32_e32 v57, 0xffff0000, v57
	v_and_b32_e32 v56, 0xffff0000, v56
	v_and_b32_e32 v49, 0xffff0000, v49
	v_and_b32_e32 v48, 0xffff0000, v48
	v_pk_fma_f32 v[46:47], v[214:215], v[92:93], v[46:47] neg_lo:[1,0,0] neg_hi:[1,0,0]
	v_pk_fma_f32 v[48:49], v[214:215], v[48:49], v[56:57] neg_lo:[1,0,0] neg_hi:[1,0,0]
	v_pk_mul_f32 v[56:57], v[46:47], v[46:47]
	v_pk_mul_f32 v[92:93], v[48:49], v[48:49]
	v_mov_b32_e32 v85, v56
	v_mov_b32_e32 v87, v92
	v_mov_b32_e32 v89, v57
	v_mov_b32_e32 v91, v93
	v_pk_add_f32 v[84:85], v[84:85], v[86:87]
	v_pk_add_f32 v[56:57], v[88:89], v[90:91]
	v_mov_b32_e32 v10, v9
	v_pk_add_f32 v[56:57], v[84:85], v[56:57]
	s_nop 0
	v_add_f32_e32 v56, v56, v57
	ds_bpermute_b32 v57, v83, v56
	s_waitcnt lgkmcnt(0)
	v_add_f32_e32 v2, v56, v57
	v_fmamk_f32 v2, v2, 0x3c000000, v1
	v_mul_f32_e32 v14, 0x4f800000, v2
	v_cmp_gt_f32_e32 vcc, s0, v2
	s_nop 1
	v_cndmask_b32_e32 v2, v2, v14, vcc
	v_sqrt_f32_e32 v56, v2
	v_mov_b32_e32 v14, v8
	v_add_u32_e32 v8, -1, v56
	v_fma_f32 v9, -v8, v56, v2
	v_cmp_ge_f32_e64 s[0:1], 0, v9
	v_add_u32_e32 v9, 1, v56
	s_nop 0
	v_cndmask_b32_e64 v8, v56, v8, s[0:1]
	v_fma_f32 v56, -v9, v56, v2
	v_cmp_lt_f32_e64 s[0:1], 0, v56
	s_nop 1
	v_cndmask_b32_e64 v8, v8, v9, s[0:1]
	v_mul_f32_e32 v9, 0x37800000, v8
	v_cndmask_b32_e32 v8, v8, v9, vcc
	v_cmp_class_f32_e32 vcc, v2, v226
	v_mov_b32_e32 v9, v6
	v_mov_b32_e32 v6, v5
	v_cndmask_b32_e32 v2, v8, v2, vcc
	v_div_scale_f32 v56, s[0:1], v2, v2, 1.0
	v_rcp_f32_e32 v57, v56
	v_mov_b32_e32 v8, v4
	v_fma_f32 v4, -v56, v57, 1.0
	v_fmac_f32_e32 v57, v4, v57
	v_div_scale_f32 v4, vcc, 1.0, v2, 1.0
	v_mul_f32_e32 v5, v4, v57
	v_fma_f32 v83, -v56, v5, v4
	v_fmac_f32_e32 v5, v83, v57
	v_fma_f32 v4, -v56, v5, v4
	v_div_fmas_f32 v4, v4, v57, v5
	v_div_fixup_f32 v2, v4, v2, 1.0
	v_mul_f32_e32 v2, 0x3f4ccccd, v2
	v_pk_mul_f32 v[4:5], v[78:79], v[2:3] op_sel_hi:[1,0]
	v_pk_mul_f32 v[16:17], v[16:17], v[2:3] op_sel_hi:[1,0]
	v_pk_mul_f32 v[4:5], v[14:15], v[4:5]
	v_pk_mul_f32 v[14:15], v[72:73], v[2:3] op_sel_hi:[1,0]
	s_nop 0
	v_pk_mul_f32 v[10:11], v[10:11], v[14:15]
	v_pk_mul_f32 v[14:15], v[70:71], v[2:3] op_sel_hi:[1,0]
	v_pk_mul_f32 v[8:9], v[8:9], v[14:15]
	v_pk_mul_f32 v[14:15], v[64:65], v[2:3] op_sel_hi:[1,0]
	v_pk_mul_f32 v[6:7], v[6:7], v[14:15]
	v_cvt_pk_bf16_f32 v7, v9, v7
	v_cvt_pk_bf16_f32 v6, v8, v6
	v_cvt_pk_bf16_f32 v5, v5, v11
	v_cvt_pk_bf16_f32 v4, v4, v10
	global_store_dwordx4 v[12:13], v[4:7], off offset:1024
	global_load_dwordx4 v[4:7], v82, s[58:59] offset:32
	s_nop 0
	global_load_dwordx4 v[8:11], v82, s[58:59] offset:48
	v_pk_mul_f32 v[14:15], v[18:19], v[2:3] op_sel_hi:[1,0]
	s_waitcnt vmcnt(1)
	v_mov_b32_e32 v19, v6
	v_mov_b32_e32 v6, v5
	v_mov_b32_e32 v18, v4
	v_pk_mul_f32 v[4:5], v[6:7], v[16:17]
	v_pk_mul_f32 v[6:7], v[40:41], v[2:3] op_sel_hi:[1,0]
	s_waitcnt vmcnt(0)
	v_mov_b32_e32 v16, v8
	v_mov_b32_e32 v17, v10
	v_pk_mul_f32 v[6:7], v[16:17], v[6:7]
	v_pk_mul_f32 v[16:17], v[50:51], v[2:3] op_sel_hi:[1,0]
	v_mov_b32_e32 v10, v9
	v_pk_mul_f32 v[8:9], v[10:11], v[16:17]
	v_pk_mul_f32 v[14:15], v[18:19], v[14:15]
	v_bfe_u32 v10, v9, 16, 1
	v_bfe_u32 v11, v8, 16, 1
	v_add3_u32 v8, v8, v11, s81
	v_add3_u32 v9, v9, v10, s81
	v_bfe_u32 v16, v6, 16, 1
	v_bfe_u32 v17, v7, 16, 1
	v_add3_u32 v7, v7, v17, s81
	v_add3_u32 v6, v6, v16, s81
	v_lshrrev_b32_e32 v6, 16, v6
	v_lshrrev_b32_e32 v7, 16, v7
	v_and_or_b32 v7, v9, s80, v7
	v_and_or_b32 v6, v8, s80, v6
	v_cvt_pk_bf16_f32 v5, v15, v5
	v_cvt_pk_bf16_f32 v4, v14, v4
	global_store_dwordx4 v[12:13], v[4:7], off offset:1040
	global_load_dwordx4 v[4:7], v82, s[58:59] offset:64
	s_nop 0
	global_load_dwordx4 v[8:11], v82, s[58:59] offset:80
	v_pk_mul_f32 v[14:15], v[26:27], v[2:3] op_sel_hi:[1,0]
	v_pk_mul_f32 v[18:19], v[62:63], v[2:3] op_sel_hi:[1,0]
	s_waitcnt vmcnt(1)
	v_mov_b32_e32 v16, v4
	v_mov_b32_e32 v17, v6
	v_pk_mul_f32 v[14:15], v[14:15], v[16:17]
	v_pk_mul_f32 v[16:17], v[34:35], v[2:3] op_sel_hi:[1,0]
	v_mov_b32_e32 v6, v5
	v_pk_mul_f32 v[4:5], v[16:17], v[6:7]
	v_pk_mul_f32 v[6:7], v[42:43], v[2:3] op_sel_hi:[1,0]
	s_waitcnt vmcnt(0)
	v_mov_b32_e32 v16, v8
	v_mov_b32_e32 v17, v10
	v_pk_mul_f32 v[6:7], v[6:7], v[16:17]
	v_pk_mul_f32 v[16:17], v[54:55], v[2:3] op_sel_hi:[1,0]
	v_mov_b32_e32 v10, v9
	v_pk_mul_f32 v[8:9], v[16:17], v[10:11]
	v_bfe_u32 v10, v9, 16, 1
	v_bfe_u32 v11, v8, 16, 1
	v_add3_u32 v8, v8, v11, s81
	v_add3_u32 v9, v9, v10, s81
	v_bfe_u32 v16, v6, 16, 1
	v_bfe_u32 v17, v7, 16, 1
	v_add3_u32 v7, v7, v17, s81
	v_add3_u32 v6, v6, v16, s81
	v_lshrrev_b32_e32 v6, 16, v6
	v_lshrrev_b32_e32 v7, 16, v7
	v_and_or_b32 v7, v9, s80, v7
	v_and_or_b32 v6, v8, s80, v6
	v_cvt_pk_bf16_f32 v5, v15, v5
	v_cvt_pk_bf16_f32 v4, v14, v4
	global_store_dwordx4 v[12:13], v[4:7], off offset:1056
	global_load_dwordx4 v[4:7], v82, s[58:59] offset:96
	s_nop 0
	global_load_dwordx4 v[8:11], v82, s[58:59] offset:112
	v_pk_mul_f32 v[14:15], v[24:25], v[2:3] op_sel_hi:[1,0]
	v_pk_mul_f32 v[24:25], v[76:77], v[2:3] op_sel_hi:[1,0]
	s_waitcnt vmcnt(1)
	v_mov_b32_e32 v16, v4
	v_mov_b32_e32 v17, v6
	v_pk_mul_f32 v[14:15], v[14:15], v[16:17]
	v_pk_mul_f32 v[16:17], v[30:31], v[2:3] op_sel_hi:[1,0]
	v_mov_b32_e32 v6, v5
	v_pk_mul_f32 v[4:5], v[16:17], v[6:7]
	v_pk_mul_f32 v[6:7], v[60:61], v[2:3] op_sel_hi:[1,0]
	s_waitcnt vmcnt(0)
	v_mov_b32_e32 v16, v8
	v_mov_b32_e32 v17, v10
	v_pk_mul_f32 v[6:7], v[6:7], v[16:17]
	v_pk_mul_f32 v[16:17], v[74:75], v[2:3] op_sel_hi:[1,0]
	v_mov_b32_e32 v10, v9
	v_pk_mul_f32 v[8:9], v[16:17], v[10:11]
	v_bfe_u32 v10, v9, 16, 1
	v_bfe_u32 v11, v8, 16, 1
	v_add3_u32 v8, v8, v11, s81
	v_add3_u32 v9, v9, v10, s81
	v_bfe_u32 v16, v6, 16, 1
	v_bfe_u32 v17, v7, 16, 1
	v_add3_u32 v7, v7, v17, s81
	v_add3_u32 v6, v6, v16, s81
	v_lshrrev_b32_e32 v6, 16, v6
	v_lshrrev_b32_e32 v7, 16, v7
	v_and_or_b32 v7, v9, s80, v7
	v_and_or_b32 v6, v8, s80, v6
	v_cvt_pk_bf16_f32 v5, v15, v5
	v_cvt_pk_bf16_f32 v4, v14, v4
	global_store_dwordx4 v[12:13], v[4:7], off offset:1072
	global_load_dwordx4 v[4:7], v82, s[58:59] offset:128
	s_nop 0
	global_load_dwordx4 v[8:11], v82, s[58:59] offset:144
	v_pk_mul_f32 v[14:15], v[28:29], v[2:3] op_sel_hi:[1,0]
	s_waitcnt vmcnt(1)
	v_mov_b32_e32 v16, v4
	v_mov_b32_e32 v17, v6
	v_pk_mul_f32 v[14:15], v[14:15], v[16:17]
	v_pk_mul_f32 v[16:17], v[36:37], v[2:3] op_sel_hi:[1,0]
	v_mov_b32_e32 v6, v5
	v_pk_mul_f32 v[4:5], v[16:17], v[6:7]
	v_pk_mul_f32 v[6:7], v[58:59], v[2:3] op_sel_hi:[1,0]
	s_waitcnt vmcnt(0)
	v_mov_b32_e32 v16, v8
	v_mov_b32_e32 v17, v10
	v_pk_mul_f32 v[6:7], v[6:7], v[16:17]
	v_pk_mul_f32 v[16:17], v[66:67], v[2:3] op_sel_hi:[1,0]
	v_mov_b32_e32 v10, v9
	v_pk_mul_f32 v[8:9], v[16:17], v[10:11]
	v_bfe_u32 v10, v9, 16, 1
	v_bfe_u32 v11, v8, 16, 1
	v_add3_u32 v8, v8, v11, s81
	v_add3_u32 v9, v9, v10, s81
	v_bfe_u32 v16, v6, 16, 1
	v_bfe_u32 v17, v7, 16, 1
	v_add3_u32 v7, v7, v17, s81
	v_add3_u32 v6, v6, v16, s81
	v_lshrrev_b32_e32 v6, 16, v6
	v_lshrrev_b32_e32 v7, 16, v7
	v_and_or_b32 v7, v9, s80, v7
	v_and_or_b32 v6, v8, s80, v6
	v_cvt_pk_bf16_f32 v5, v15, v5
	v_cvt_pk_bf16_f32 v4, v14, v4
	global_store_dwordx4 v[12:13], v[4:7], off offset:1088
	global_load_dwordx4 v[4:7], v82, s[58:59] offset:160
	s_nop 0
	global_load_dwordx4 v[8:11], v82, s[58:59] offset:176
	v_pk_mul_f32 v[16:17], v[52:53], v[2:3] op_sel_hi:[1,0]
	v_pk_mul_f32 v[14:15], v[44:45], v[2:3] op_sel_hi:[1,0]
	s_waitcnt vmcnt(1)
	v_mov_b32_e32 v27, v6
	v_mov_b32_e32 v6, v5
	s_waitcnt vmcnt(0)
	v_mov_b32_e32 v5, v10
	v_mov_b32_e32 v10, v9
	v_mov_b32_e32 v26, v4
	v_mov_b32_e32 v4, v8
	v_pk_mul_f32 v[6:7], v[16:17], v[6:7]
	v_pk_mul_f32 v[10:11], v[24:25], v[10:11]
	v_pk_mul_f32 v[8:9], v[14:15], v[26:27]
	v_pk_mul_f32 v[4:5], v[18:19], v[4:5]
	v_bfe_u32 v14, v11, 16, 1
	v_bfe_u32 v15, v10, 16, 1
	v_bfe_u32 v16, v7, 16, 1
	v_bfe_u32 v17, v6, 16, 1
	v_add3_u32 v17, v6, v17, s81
	v_add3_u32 v16, v7, v16, s81
	v_add3_u32 v6, v10, v15, s81
	v_add3_u32 v7, v11, v14, s81
	v_bfe_u32 v10, v8, 16, 1
	v_bfe_u32 v11, v9, 16, 1
	v_bfe_u32 v14, v4, 16, 1
	v_bfe_u32 v15, v5, 16, 1
	v_add3_u32 v5, v5, v15, s81
	v_add3_u32 v4, v4, v14, s81
	v_add3_u32 v9, v9, v11, s81
	v_add3_u32 v8, v8, v10, s81
	v_lshrrev_b32_e32 v8, 16, v8
	v_lshrrev_b32_e32 v9, 16, v9
	v_lshrrev_b32_e32 v4, 16, v4
	v_lshrrev_b32_e32 v5, 16, v5
	v_and_or_b32 v7, v7, s80, v5
	v_and_or_b32 v6, v6, s80, v4
	v_and_or_b32 v5, v16, s80, v9
	v_and_or_b32 v4, v17, s80, v8
	global_store_dwordx4 v[12:13], v[4:7], off offset:1104
	global_load_dwordx4 v[4:7], v82, s[58:59] offset:192
	s_nop 0
	global_load_dwordx4 v[8:11], v82, s[58:59] offset:208
	v_pk_mul_f32 v[14:15], v[32:33], v[2:3] op_sel_hi:[1,0]
	v_pk_mul_f32 v[18:19], v[68:69], v[2:3] op_sel_hi:[1,0]
	v_pk_mul_f32 v[16:17], v[38:39], v[2:3] op_sel_hi:[1,0]
	v_pk_mul_f32 v[24:25], v[80:81], v[2:3] op_sel_hi:[1,0]
	s_waitcnt vmcnt(1)
	v_mov_b32_e32 v26, v4
	v_mov_b32_e32 v27, v6
	v_mov_b32_e32 v6, v5
	s_waitcnt vmcnt(0)
	v_mov_b32_e32 v4, v8
	v_mov_b32_e32 v5, v10
	v_mov_b32_e32 v10, v9
	v_pk_mul_f32 v[8:9], v[14:15], v[26:27]
	v_pk_mul_f32 v[4:5], v[18:19], v[4:5]
	v_pk_mul_f32 v[6:7], v[16:17], v[6:7]
	v_pk_mul_f32 v[10:11], v[24:25], v[10:11]
	v_bfe_u32 v18, v8, 16, 1
	v_bfe_u32 v19, v9, 16, 1
	v_bfe_u32 v16, v7, 16, 1
	v_bfe_u32 v17, v6, 16, 1
	v_add3_u32 v9, v9, v19, s81
	v_add3_u32 v8, v8, v18, s81
	v_add3_u32 v17, v6, v17, s81
	v_add3_u32 v16, v7, v16, s81
	v_lshrrev_b32_e32 v8, 16, v8
	v_lshrrev_b32_e32 v9, 16, v9
	v_cvt_pk_bf16_f32 v7, v5, v11
	v_cvt_pk_bf16_f32 v6, v4, v10
	v_and_or_b32 v5, v16, s80, v9
	v_and_or_b32 v4, v17, s80, v8
	global_store_dwordx4 v[12:13], v[4:7], off offset:1120
	global_load_dwordx4 v[4:7], v82, s[58:59] offset:224
	s_nop 0
	global_load_dwordx4 v[8:11], v82, s[58:59] offset:240
	v_pk_mul_f32 v[14:15], v[20:21], v[2:3] op_sel_hi:[1,0]
	v_pk_mul_f32 v[16:17], v[22:23], v[2:3] op_sel_hi:[1,0]
	v_pk_mul_f32 v[18:19], v[46:47], v[2:3] op_sel_hi:[1,0]
	v_pk_mul_f32 v[20:21], v[48:49], v[2:3] op_sel_hi:[1,0]
	s_waitcnt vmcnt(1)
	v_mov_b32_e32 v22, v4
	v_mov_b32_e32 v23, v6
	v_mov_b32_e32 v6, v5
	s_waitcnt vmcnt(0)
	v_mov_b32_e32 v4, v8
	v_mov_b32_e32 v5, v10
	v_mov_b32_e32 v10, v9
	v_pk_mul_f32 v[8:9], v[14:15], v[22:23]
	v_pk_mul_f32 v[6:7], v[16:17], v[6:7]
	v_pk_mul_f32 v[4:5], v[18:19], v[4:5]
	v_pk_mul_f32 v[10:11], v[20:21], v[10:11]
	v_bfe_u32 v15, v7, 16, 1
	v_bfe_u32 v17, v8, 16, 1
	v_bfe_u32 v18, v9, 16, 1
	v_bfe_u32 v19, v4, 16, 1
	v_bfe_u32 v14, v10, 16, 1
	v_bfe_u32 v16, v6, 16, 1
	v_add3_u32 v15, v7, v15, s81
	v_add3_u32 v4, v4, v19, s81
	v_add3_u32 v7, v9, v18, s81
	v_add3_u32 v8, v8, v17, s81
	v_add3_u32 v16, v6, v16, s81
	v_add3_u32 v6, v10, v14, s81
	v_lshrrev_b32_e32 v8, 16, v8
	v_lshrrev_b32_e32 v9, 16, v7
	v_lshrrev_b32_e32 v4, 16, v4
	v_cvt_pk_bf16_f32 v7, v5, v11
	v_and_or_b32 v6, v6, s80, v4
	v_and_or_b32 v5, v15, s80, v9
	v_and_or_b32 v4, v16, s80, v8
	global_store_dwordx4 v[12:13], v[4:7], off offset:1136
	s_branch .LBB0_259

.Lfin_skip_l0:
	v_mov_b32_e32 v2, v243
	v_mov_b32_e32 v8, v243
	s_nop 1
	v_permlane32_swap_b32_e32 v2, v8
	v_cmp_gt_u32_e32 vcc, 32, v230
	s_branch .Lfin_join_l0
	s_nop 0
	s_nop 0
	s_nop 0
	s_nop 0
	s_nop 0
	s_nop 0
	s_nop 0
	s_nop 0

.LBB0_952:
	s_cmp_lt_u32 s33, 4
	s_cbranch_scc1 .Lfin_skip_l1
	v_add_u32_e32 v2, s43, v242
	ds_read_b64_tr_b16 v[194:195], v2 offset:24576
	ds_read_b64_tr_b16 v[196:197], v2 offset:25088
	s_waitcnt lgkmcnt(9)
	v_mfma_f32_32x32x16_bf16 v[82:97], v[170:173], v[154:157], v[100:115]
	ds_read_b64_tr_b16 v[170:171], v2 offset:28672
	ds_read_b64_tr_b16 v[172:173], v2 offset:29184
	s_waitcnt lgkmcnt(10)
	v_mfma_f32_32x32x16_bf16 v[100:115], v[162:165], v[154:157], v[100:115]
	ds_read_b64_tr_b16 v[124:125], v2 offset:25600
	ds_read_b64_tr_b16 v[126:127], v2 offset:26112
	s_waitcnt lgkmcnt(11)
	v_mfma_f32_32x32x16_bf16 v[82:97], v[174:177], v[150:153], v[82:97]
	ds_read_b64_tr_b16 v[120:121], v2 offset:29696
	ds_read_b64_tr_b16 v[122:123], v2 offset:30208
	s_waitcnt lgkmcnt(12)
	v_mfma_f32_32x32x16_bf16 v[100:115], v[166:169], v[150:153], v[100:115]
	ds_read_b64_tr_b16 v[116:117], v2 offset:26624
	ds_read_b64_tr_b16 v[118:119], v2 offset:27136
	s_waitcnt lgkmcnt(13)
	v_mfma_f32_32x32x16_bf16 v[82:97], v[182:185], v[146:149], v[82:97]
	ds_read_b64_tr_b16 v[12:13], v2 offset:30720
	ds_read_b64_tr_b16 v[14:15], v2 offset:31232
	s_waitcnt lgkmcnt(14)
	v_mfma_f32_32x32x16_bf16 v[100:115], v[178:181], v[146:149], v[100:115]
	ds_read_b64_tr_b16 v[8:9], v2 offset:27648
	ds_read_b64_tr_b16 v[10:11], v2 offset:28160
	s_waitcnt lgkmcnt(14)
	v_mfma_f32_32x32x16_bf16 v[82:97], v[190:193], v[142:145], v[82:97]
	ds_read_b64_tr_b16 v[4:5], v2 offset:31744
	ds_read_b64_tr_b16 v[6:7], v2 offset:32256
	v_mfma_f32_32x32x16_bf16 v[100:115], v[186:189], v[142:145], v[100:115]
	v_or_b32_e32 v17, 0xe0, v239
	v_or_b32_e32 v16, 0xc0, v239
	v_cmp_le_i32_e32 vcc, v17, v238
	s_nop 8
	v_cndmask_b32_e32 v99, v227, v100, vcc
	v_cmp_lt_i32_e32 vcc, v16, v238
	s_nop 1
	v_cndmask_b32_e32 v83, v227, v83, vcc
	v_cmp_le_i32_e32 vcc, v16, v238
	v_or_b32_e32 v16, 0xe1, v239
	s_nop 0
	v_cndmask_b32_e32 v82, v227, v82, vcc
	v_cmp_le_i32_e32 vcc, v16, v238
	v_or_b32_e32 v16, 0xc2, v239
	s_nop 0
	v_cndmask_b32_e32 v100, v227, v101, vcc
	v_cmp_le_i32_e32 vcc, v16, v238
	v_or_b32_e32 v16, 0xe2, v239
	s_nop 0
	v_cndmask_b32_e32 v101, v227, v84, vcc
	v_cmp_le_i32_e32 vcc, v16, v238
	v_or_b32_e32 v16, 0xc3, v239
	s_nop 0
	v_cndmask_b32_e32 v142, v227, v102, vcc
	v_cmp_le_i32_e32 vcc, v16, v238
	v_or_b32_e32 v16, 0xe3, v239
	s_nop 0
	v_cndmask_b32_e32 v143, v227, v85, vcc
	v_cmp_le_i32_e32 vcc, v16, v238
	v_or_b32_e32 v16, 0xc8, v239
	s_nop 0
	v_cndmask_b32_e32 v144, v227, v103, vcc
	v_cmp_le_i32_e32 vcc, v16, v238
	v_or_b32_e32 v16, 0xe8, v239
	s_nop 0
	v_cndmask_b32_e32 v102, v227, v86, vcc
	v_cmp_le_i32_e32 vcc, v16, v238
	v_or_b32_e32 v16, 0xc9, v239
	s_nop 0
	v_cndmask_b32_e32 v86, v227, v104, vcc
	v_cmp_le_i32_e32 vcc, v16, v238
	v_or_b32_e32 v16, 0xe9, v239
	s_nop 0
	v_cndmask_b32_e32 v103, v227, v87, vcc
	v_cmp_le_i32_e32 vcc, v16, v238
	v_or_b32_e32 v16, 0xca, v239
	s_nop 0
	v_cndmask_b32_e32 v87, v227, v105, vcc
	v_cmp_le_i32_e32 vcc, v16, v238
	v_or_b32_e32 v16, 0xea, v239
	s_nop 0
	v_cndmask_b32_e32 v104, v227, v88, vcc
	v_cmp_le_i32_e32 vcc, v16, v238
	v_or_b32_e32 v16, 0xcb, v239
	s_nop 0
	v_cndmask_b32_e32 v88, v227, v106, vcc
	v_cmp_le_i32_e32 vcc, v16, v238
	v_or_b32_e32 v16, 0xeb, v239
	s_nop 0
	v_cndmask_b32_e32 v105, v227, v89, vcc
	v_cmp_le_i32_e32 vcc, v16, v238
	v_or_b32_e32 v16, 0xd0, v239
	s_nop 0
	v_cndmask_b32_e32 v89, v227, v107, vcc
	v_cmp_le_i32_e32 vcc, v16, v238
	v_or_b32_e32 v16, 0xf0, v239
	s_nop 0
	v_cndmask_b32_e32 v106, v227, v90, vcc
	v_cmp_le_i32_e32 vcc, v16, v238
	v_or_b32_e32 v16, 0xd1, v239
	s_nop 0
	v_cndmask_b32_e32 v90, v227, v108, vcc
	v_cmp_le_i32_e32 vcc, v16, v238
	v_or_b32_e32 v16, 0xf1, v239
	s_nop 0
	v_cndmask_b32_e32 v107, v227, v91, vcc
	v_cmp_le_i32_e32 vcc, v16, v238
	v_or_b32_e32 v16, 0xd2, v239
	s_nop 0
	v_cndmask_b32_e32 v91, v227, v109, vcc
	v_cmp_le_i32_e32 vcc, v16, v238
	v_or_b32_e32 v16, 0xf2, v239
	s_nop 0
	v_cndmask_b32_e32 v108, v227, v92, vcc
	v_cmp_le_i32_e32 vcc, v16, v238
	v_or_b32_e32 v16, 0xd3, v239
	s_nop 0
	v_cndmask_b32_e32 v92, v227, v110, vcc
	v_cmp_le_i32_e32 vcc, v16, v238
	v_or_b32_e32 v16, 0xf3, v239
	s_nop 0
	v_cndmask_b32_e32 v109, v227, v93, vcc
	v_cmp_le_i32_e32 vcc, v16, v238
	v_or_b32_e32 v16, 0xd8, v239
	s_nop 0
	v_cndmask_b32_e32 v93, v227, v111, vcc
	v_cmp_le_i32_e32 vcc, v16, v238
	v_or_b32_e32 v16, 0xf8, v239
	s_nop 0
	v_cndmask_b32_e32 v110, v227, v94, vcc
	v_cmp_le_i32_e32 vcc, v16, v238
	v_or_b32_e32 v16, 0xd9, v239
	s_nop 0
	v_cndmask_b32_e32 v94, v227, v112, vcc
	v_cmp_le_i32_e32 vcc, v16, v238
	v_or_b32_e32 v16, 0xf9, v239
	s_nop 0
	v_cndmask_b32_e32 v111, v227, v95, vcc
	v_cmp_le_i32_e32 vcc, v16, v238
	v_or_b32_e32 v16, 0xda, v239
	s_nop 0
	v_cndmask_b32_e32 v95, v227, v113, vcc
	v_cmp_le_i32_e32 vcc, v16, v238
	v_or_b32_e32 v16, 0xfa, v239
	s_nop 0
	v_cndmask_b32_e32 v112, v227, v96, vcc
	v_cmp_le_i32_e32 vcc, v16, v238
	v_or_b32_e32 v16, 0xdb, v239
	s_nop 0
	v_cndmask_b32_e32 v96, v227, v114, vcc
	v_cmp_le_i32_e32 vcc, v16, v238
	v_sub_u32_e32 v16, v238, v239
	v_lshl_add_u32 v145, v16, 2, s40
	v_cndmask_b32_e32 v113, v227, v97, vcc
	v_or_b32_e32 v97, 0xfb, v239
	v_cmp_le_i32_e32 vcc, v97, v238
	ds_read2_b32 v[16:17], v145 offset0:63 offset1:64
	ds_read2_b32 v[84:85], v145 offset0:31 offset1:32
	v_cndmask_b32_e32 v97, v227, v115, vcc
	ds_read2_b32 v[114:115], v145 offset0:61 offset1:62
	ds_read2_b32 v[128:129], v145 offset0:29 offset1:30
	s_waitcnt lgkmcnt(3)
	v_add_f32_e32 v98, v82, v17
	s_waitcnt lgkmcnt(2)
	v_add_f32_e32 v82, v99, v85
	v_add_f32_e32 v99, v83, v16
	v_add_f32_e32 v83, v100, v84
	s_waitcnt lgkmcnt(1)
	v_add_f32_e32 v100, v101, v115
	s_waitcnt lgkmcnt(0)
	v_add_f32_e32 v84, v142, v129
	v_add_f32_e32 v101, v143, v114
	v_add_f32_e32 v85, v144, v128
	s_nop 0
	ds_read2_b32 v[16:17], v145 offset0:55 offset1:56
	ds_read2_b32 v[114:115], v145 offset0:23 offset1:24
	ds_read2_b32 v[128:129], v145 offset0:53 offset1:54
	ds_read2_b32 v[142:143], v145 offset0:21 offset1:22
	s_waitcnt lgkmcnt(3)
	v_add_f32_e32 v102, v102, v17
	s_waitcnt lgkmcnt(2)
	v_add_f32_e32 v86, v86, v115
	v_add_f32_e32 v103, v103, v16
	v_add_f32_e32 v87, v87, v114
	s_waitcnt lgkmcnt(1)
	v_add_f32_e32 v104, v104, v129
	s_waitcnt lgkmcnt(0)
	v_add_f32_e32 v88, v88, v143
	v_add_f32_e32 v105, v105, v128
	v_add_f32_e32 v89, v89, v142
	s_nop 0
	ds_read2_b32 v[16:17], v145 offset0:47 offset1:48
	ds_read2_b32 v[114:115], v145 offset0:15 offset1:16
	ds_read2_b32 v[128:129], v145 offset0:45 offset1:46
	ds_read2_b32 v[142:143], v145 offset0:13 offset1:14
	s_waitcnt lgkmcnt(3)
	v_add_f32_e32 v106, v106, v17
	s_waitcnt lgkmcnt(2)
	v_add_f32_e32 v90, v90, v115
	v_add_f32_e32 v107, v107, v16
	v_add_f32_e32 v91, v91, v114
	s_waitcnt lgkmcnt(1)
	v_add_f32_e32 v108, v108, v129
	s_waitcnt lgkmcnt(0)
	v_add_f32_e32 v92, v92, v143
	v_add_f32_e32 v109, v109, v128
	v_add_f32_e32 v93, v93, v142
	s_nop 0
	ds_read2_b32 v[16:17], v145 offset0:39 offset1:40
	ds_read2_b32 v[114:115], v145 offset0:7 offset1:8
	ds_read2_b32 v[128:129], v145 offset0:37 offset1:38
	ds_read2_b32 v[142:143], v145 offset0:5 offset1:6
	s_waitcnt lgkmcnt(3)
	v_add_f32_e32 v110, v110, v17
	s_waitcnt lgkmcnt(2)
	v_add_f32_e32 v94, v94, v115
	v_add_f32_e32 v111, v111, v16
	v_add_f32_e32 v95, v95, v114
	s_waitcnt lgkmcnt(1)
	v_add_f32_e32 v112, v112, v129
	s_waitcnt lgkmcnt(0)
	v_add_f32_e32 v96, v96, v143
	v_add_f32_e32 v113, v113, v128
	v_add_f32_e32 v97, v97, v142
	s_nop 0
	s_nop 0
	v_max_f32_e32 v16, v99, v98
	v_max3_f32 v17, v100, v101, v83
	v_max3_f32 v16, v16, v82, v84
	v_max3_f32 v16, v16, v85, v102
	v_max3_f32 v17, v17, v104, v105
	v_max3_f32 v16, v16, v103, v86
	v_max3_f32 v17, v17, v88, v89
	v_max3_f32 v16, v16, v87, v106
	v_max3_f32 v17, v17, v108, v109
	v_max3_f32 v16, v16, v107, v90
	v_max3_f32 v17, v17, v92, v93
	v_max3_f32 v16, v16, v91, v110
	v_max3_f32 v17, v17, v112, v113
	v_max3_f32 v16, v16, v111, v94
	v_max3_f32 v17, v17, v96, v97
	v_max3_f32 v16, v16, v95, v17
	v_mov_b32_e32 v17, v16
	s_nop 1
	v_permlane32_swap_b32_e32 v16, v17
	v_max_f32_e32 v16, v16, v17
	v_cmp_lt_f32_e32 vcc, s60, v16
	s_cmp_lg_u64 vcc, 0
	s_cselect_b64 s[0:1], -1, 0
	s_cbranch_vccnz .LBB0_959

.Lfin_join_l1:
	s_and_saveexec_b64 s[0:1], vcc
	v_add_f32_e32 v2, v2, v8
	ds_write_b32 v235, v2 offset:128
	s_or_b64 exec, exec, s[0:1]
	s_waitcnt lgkmcnt(0)
	ds_read_b128 v[4:7], v234 offset:128
	ds_read_b128 v[8:11], v234 offset:160
	s_lshl_b32 s0, s42, 8
	s_add_u32 s2, s6, s0
	s_addc_u32 s3, s7, 0
	s_waitcnt lgkmcnt(1)
	v_rcp_f32_e32 v14, v4
	v_rcp_f32_e32 v15, v5
	v_rcp_f32_e32 v16, v6
	v_rcp_f32_e32 v17, v7
	ds_read_b128 v[4:7], v234 offset:192
	s_lshl_b64 s[0:1], s[26:27], 11
	s_add_u32 s0, s2, s0
	s_addc_u32 s1, s3, s1
	s_lshl_b32 s2, s33, 12
	s_add_i32 s2, s2, 0
	v_lshlrev_b32_e32 v2, 1, v232
	s_add_i32 s2, s2, 0x16800
	v_and_b32_e32 v2, 0x70, v2
	s_waitcnt lgkmcnt(1)
	v_rcp_f32_e32 v82, v8
	v_rcp_f32_e32 v83, v9
	v_rcp_f32_e32 v84, v10
	v_rcp_f32_e32 v85, v11
	ds_read_b128 v[8:11], v234 offset:224
	s_waitcnt lgkmcnt(1)
	v_rcp_f32_e32 v86, v4
	v_lshlrev_b32_e32 v4, 1, v231
	v_add_u32_e32 v95, s2, v2
	v_lshl_add_u64 v[12:13], s[0:1], 0, v[2:3]
	v_lshlrev_b32_e32 v2, 9, v229
	v_add3_u32 v97, s2, v4, v2
	v_mul_f32_e32 v2, v66, v14
	v_cvt_pk_bf16_f32 v2, v2, s0
	ds_write_b16 v97, v2
	v_mul_f32_e32 v2, v50, v14
	v_cvt_pk_bf16_f32 v2, v2, s0
	ds_write_b16 v97, v2 offset:64
	v_mul_f32_e32 v2, v67, v15
	v_cvt_pk_bf16_f32 v2, v2, s0
	ds_write_b16 v97, v2 offset:128
	v_mul_f32_e32 v2, v51, v15
	v_cvt_pk_bf16_f32 v2, v2, s0
	ds_write_b16 v97, v2 offset:192
	v_mul_f32_e32 v2, v68, v16
	v_cvt_pk_bf16_f32 v2, v2, s0
	ds_write_b16 v97, v2 offset:256
	v_mul_f32_e32 v2, v52, v16
	v_cvt_pk_bf16_f32 v2, v2, s0
	ds_write_b16 v97, v2 offset:320
	v_mul_f32_e32 v2, v69, v17
	v_cvt_pk_bf16_f32 v2, v2, s0
	ds_write_b16 v97, v2 offset:384
	v_mul_f32_e32 v2, v53, v17
	v_cvt_pk_bf16_f32 v2, v2, s0
	ds_write_b16 v97, v2 offset:448
	v_mul_f32_e32 v2, v70, v82
	v_cvt_pk_bf16_f32 v2, v2, s0
	ds_write_b16 v97, v2 offset:1024
	v_mul_f32_e32 v2, v54, v82
	v_cvt_pk_bf16_f32 v2, v2, s0
	ds_write_b16 v97, v2 offset:1088
	v_mul_f32_e32 v2, v71, v83
	v_cvt_pk_bf16_f32 v2, v2, s0
	ds_write_b16 v97, v2 offset:1152
	v_mul_f32_e32 v2, v55, v83
	v_cvt_pk_bf16_f32 v2, v2, s0
	ds_write_b16 v97, v2 offset:1216
	v_mul_f32_e32 v2, v72, v84
	v_cvt_pk_bf16_f32 v2, v2, s0
	ds_write_b16 v97, v2 offset:1280
	v_mul_f32_e32 v2, v56, v84
	v_cvt_pk_bf16_f32 v2, v2, s0
	ds_write_b16 v97, v2 offset:1344
	v_mul_f32_e32 v2, v73, v85
	v_cvt_pk_bf16_f32 v2, v2, s0
	ds_write_b16 v97, v2 offset:1408
	v_mul_f32_e32 v2, v57, v85
	v_cvt_pk_bf16_f32 v2, v2, s0
	v_rcp_f32_e32 v87, v5
	ds_write_b16 v97, v2 offset:1472
	v_mul_f32_e32 v2, v74, v86
	v_cvt_pk_bf16_f32 v2, v2, s0
	ds_write_b16 v97, v2 offset:2048
	v_mul_f32_e32 v2, v58, v86
	v_cvt_pk_bf16_f32 v2, v2, s0
	v_rcp_f32_e32 v88, v6
	ds_write_b16 v97, v2 offset:2112
	v_mul_f32_e32 v2, v75, v87
	v_cvt_pk_bf16_f32 v2, v2, s0
	ds_write_b16 v97, v2 offset:2176
	v_mul_f32_e32 v2, v59, v87
	v_cvt_pk_bf16_f32 v2, v2, s0
	v_rcp_f32_e32 v89, v7
	ds_write_b16 v97, v2 offset:2240
	v_mul_f32_e32 v2, v76, v88
	v_cvt_pk_bf16_f32 v2, v2, s0
	ds_write_b16 v97, v2 offset:2304
	v_mul_f32_e32 v2, v60, v88
	v_cvt_pk_bf16_f32 v2, v2, s0
	s_waitcnt lgkmcnt(14)
	v_rcp_f32_e32 v90, v8
	ds_write_b16 v97, v2 offset:2368
	v_mul_f32_e32 v2, v77, v89
	v_cvt_pk_bf16_f32 v2, v2, s0
	ds_write_b16 v97, v2 offset:2432
	v_mul_f32_e32 v2, v61, v89
	v_cvt_pk_bf16_f32 v2, v2, s0
	v_rcp_f32_e32 v91, v9
	ds_write_b16 v97, v2 offset:2496
	v_mul_f32_e32 v2, v78, v90
	v_cvt_pk_bf16_f32 v2, v2, s0
	ds_write_b16 v97, v2 offset:3072
	v_mul_f32_e32 v2, v62, v90
	v_cvt_pk_bf16_f32 v2, v2, s0
	v_rcp_f32_e32 v92, v10
	ds_write_b16 v97, v2 offset:3136
	v_mul_f32_e32 v2, v79, v91
	v_cvt_pk_bf16_f32 v2, v2, s0
	ds_write_b16 v97, v2 offset:3200
	v_mul_f32_e32 v2, v63, v91
	v_cvt_pk_bf16_f32 v2, v2, s0
	v_rcp_f32_e32 v93, v11
	ds_write_b16 v97, v2 offset:3264
	v_mul_f32_e32 v2, v80, v92
	v_cvt_pk_bf16_f32 v2, v2, s0
	ds_write_b16 v97, v2 offset:3328
	v_mul_f32_e32 v2, v64, v92
	v_cvt_pk_bf16_f32 v2, v2, s0
	ds_write_b16 v97, v2 offset:3392
	v_mul_f32_e32 v2, v81, v93
	v_cvt_pk_bf16_f32 v2, v2, s0
	ds_write_b16 v97, v2 offset:3456
	v_mul_f32_e32 v2, v65, v93
	v_lshrrev_b32_e32 v94, 3, v230
	v_cvt_pk_bf16_f32 v2, v2, s0
	ds_write_b16 v97, v2 offset:3520
	v_or_b32_e32 v52, 8, v94
	v_lshl_add_u32 v96, v94, 7, v95
	s_waitcnt lgkmcnt(0)
	v_lshl_add_u32 v58, v52, 7, v95
	ds_read_b128 v[4:7], v96
	ds_read_b128 v[8:11], v58
	v_lshlrev_b32_e32 v2, 11, v94
	v_lshl_add_u64 v[50:51], v[12:13], 0, v[2:3]
	v_lshlrev_b32_e32 v2, 11, v52
	v_lshl_add_u64 v[52:53], v[12:13], 0, v[2:3]
	v_or_b32_e32 v2, 16, v94
	v_or_b32_e32 v56, 24, v94
	v_lshl_add_u32 v59, v2, 7, v95
	v_lshl_add_u32 v60, v56, 7, v95
	s_waitcnt lgkmcnt(1)
	global_store_dwordx4 v[50:51], v[4:7], off
	ds_read_b128 v[4:7], v59
	s_waitcnt lgkmcnt(1)
	global_store_dwordx4 v[52:53], v[8:11], off
	ds_read_b128 v[8:11], v60
	v_lshlrev_b32_e32 v2, 11, v2
	v_lshl_add_u64 v[54:55], v[12:13], 0, v[2:3]
	v_lshlrev_b32_e32 v2, 11, v56
	v_lshl_add_u64 v[56:57], v[12:13], 0, v[2:3]
	v_mul_f32_e32 v2, v34, v14
	s_waitcnt lgkmcnt(1)
	global_store_dwordx4 v[54:55], v[4:7], off
	s_waitcnt lgkmcnt(0)
	global_store_dwordx4 v[56:57], v[8:11], off
	v_cvt_pk_bf16_f32 v2, v2, s0
	s_waitcnt lgkmcnt(0)
	ds_write_b16 v97, v2
	v_mul_f32_e32 v2, v18, v14
	v_cvt_pk_bf16_f32 v2, v2, s0
	ds_write_b16 v97, v2 offset:64
	v_mul_f32_e32 v2, v35, v15
	v_cvt_pk_bf16_f32 v2, v2, s0
	ds_write_b16 v97, v2 offset:128
	v_mul_f32_e32 v2, v19, v15
	v_cvt_pk_bf16_f32 v2, v2, s0
	ds_write_b16 v97, v2 offset:192
	v_mul_f32_e32 v2, v36, v16
	v_cvt_pk_bf16_f32 v2, v2, s0
	ds_write_b16 v97, v2 offset:256
	v_mul_f32_e32 v2, v20, v16
	v_cvt_pk_bf16_f32 v2, v2, s0
	ds_write_b16 v97, v2 offset:320
	v_mul_f32_e32 v2, v37, v17
	v_cvt_pk_bf16_f32 v2, v2, s0
	ds_write_b16 v97, v2 offset:384
	v_mul_f32_e32 v2, v21, v17
	v_cvt_pk_bf16_f32 v2, v2, s0
	ds_write_b16 v97, v2 offset:448
	v_mul_f32_e32 v2, v38, v82
	v_cvt_pk_bf16_f32 v2, v2, s0
	ds_write_b16 v97, v2 offset:1024
	v_mul_f32_e32 v2, v22, v82
	v_cvt_pk_bf16_f32 v2, v2, s0
	ds_write_b16 v97, v2 offset:1088
	v_mul_f32_e32 v2, v39, v83
	v_cvt_pk_bf16_f32 v2, v2, s0
	ds_write_b16 v97, v2 offset:1152
	v_mul_f32_e32 v2, v23, v83
	v_cvt_pk_bf16_f32 v2, v2, s0
	ds_write_b16 v97, v2 offset:1216
	v_mul_f32_e32 v2, v40, v84
	v_cvt_pk_bf16_f32 v2, v2, s0
	ds_write_b16 v97, v2 offset:1280
	v_mul_f32_e32 v2, v24, v84
	v_cvt_pk_bf16_f32 v2, v2, s0
	ds_write_b16 v97, v2 offset:1344
	v_mul_f32_e32 v2, v41, v85
	v_cvt_pk_bf16_f32 v2, v2, s0
	ds_write_b16 v97, v2 offset:1408
	v_mul_f32_e32 v2, v25, v85
	v_cvt_pk_bf16_f32 v2, v2, s0
	ds_write_b16 v97, v2 offset:1472
	v_mul_f32_e32 v2, v42, v86
	v_cvt_pk_bf16_f32 v2, v2, s0
	ds_write_b16 v97, v2 offset:2048
	v_mul_f32_e32 v2, v26, v86
	v_cvt_pk_bf16_f32 v2, v2, s0
	ds_write_b16 v97, v2 offset:2112
	v_mul_f32_e32 v2, v43, v87
	v_cvt_pk_bf16_f32 v2, v2, s0
	ds_write_b16 v97, v2 offset:2176
	v_mul_f32_e32 v2, v27, v87
	v_cvt_pk_bf16_f32 v2, v2, s0
	ds_write_b16 v97, v2 offset:2240
	v_mul_f32_e32 v2, v44, v88
	v_cvt_pk_bf16_f32 v2, v2, s0
	ds_write_b16 v97, v2 offset:2304
	v_mul_f32_e32 v2, v28, v88
	v_cvt_pk_bf16_f32 v2, v2, s0
	ds_write_b16 v97, v2 offset:2368
	v_mul_f32_e32 v2, v45, v89
	v_cvt_pk_bf16_f32 v2, v2, s0
	ds_write_b16 v97, v2 offset:2432
	v_mul_f32_e32 v2, v29, v89
	v_cvt_pk_bf16_f32 v2, v2, s0
	ds_write_b16 v97, v2 offset:2496
	v_mul_f32_e32 v2, v46, v90
	v_cvt_pk_bf16_f32 v2, v2, s0
	ds_write_b16 v97, v2 offset:3072
	v_mul_f32_e32 v2, v30, v90
	v_cvt_pk_bf16_f32 v2, v2, s0
	ds_write_b16 v97, v2 offset:3136
	v_mul_f32_e32 v2, v47, v91
	v_cvt_pk_bf16_f32 v2, v2, s0
	ds_write_b16 v97, v2 offset:3200
	v_mul_f32_e32 v2, v31, v91
	v_cvt_pk_bf16_f32 v2, v2, s0
	ds_write_b16 v97, v2 offset:3264
	v_mul_f32_e32 v2, v48, v92
	v_cvt_pk_bf16_f32 v2, v2, s0
	ds_write_b16 v97, v2 offset:3328
	v_mul_f32_e32 v2, v32, v92
	v_cvt_pk_bf16_f32 v2, v2, s0
	ds_write_b16 v97, v2 offset:3392
	v_mul_f32_e32 v2, v49, v93
	v_cvt_pk_bf16_f32 v2, v2, s0
	ds_write_b16 v97, v2 offset:3456
	v_mul_f32_e32 v2, v33, v93
	v_cvt_pk_bf16_f32 v2, v2, s0
	ds_write_b16 v97, v2 offset:3520
	s_waitcnt lgkmcnt(0)
	ds_read_b128 v[4:7], v96
	ds_read_b128 v[8:11], v58
	ds_read_b128 v[12:15], v59
	ds_read_b128 v[16:19], v60
	s_waitcnt lgkmcnt(3)
	global_store_dwordx4 v[50:51], v[4:7], off offset:128
	s_waitcnt lgkmcnt(2)
	global_store_dwordx4 v[52:53], v[8:11], off offset:128
	s_waitcnt lgkmcnt(1)
	global_store_dwordx4 v[54:55], v[12:15], off offset:128
	s_waitcnt lgkmcnt(0)
	global_store_dwordx4 v[56:57], v[16:19], off offset:128
	s_waitcnt lgkmcnt(0)
	s_waitcnt lgkmcnt(0)
	s_barrier
	s_cmp_lt_u32 s21, 2
	s_cbranch_scc1 .LBB0_872
	v_mov_b32_e32 v6, v0
	s_lshl_b32 s0, s63, 8
	v_ashrrev_i32_e32 v4, 1, v6
	s_or_b32 s0, s8, s0
	s_mov_b32 s1, s9
	v_ashrrev_i32_e32 v5, 31, v4
	v_lshl_add_u64 v[12:13], s[0:1], 0, v[4:5]
	v_lshlrev_b32_e32 v2, 6, v6
	v_lshlrev_b64 v[4:5], 11, v[12:13]
	v_and_b32_e32 v7, 64, v2
	v_lshl_add_u64 v[4:5], s[6:7], 0, v[4:5]
	v_lshlrev_b32_e32 v2, 1, v7
	v_lshl_add_u64 v[4:5], v[4:5], 0, v[2:3]
	s_waitcnt vmcnt(0)
	s_barrier
	global_load_dwordx2 v[16:17], v[4:5], off sc1
	global_load_dwordx2 v[18:19], v[4:5], off offset:256 sc1
	global_load_dwordx2 v[24:25], v[4:5], off offset:8 sc1
	global_load_dwordx2 v[26:27], v[4:5], off offset:264 sc1
	global_load_dwordx2 v[30:31], v[4:5], off offset:16 sc1
	global_load_dwordx2 v[34:35], v[4:5], off offset:272 sc1
	global_load_dwordx2 v[42:43], v[4:5], off offset:24 sc1
	global_load_dwordx2 v[50:51], v[4:5], off offset:280 sc1
	v_lshlrev_b32_e32 v6, 2, v6
	v_bitop3_b32 v83, v6, 4, v228 bitop3:0x6c
	v_lshlrev_b32_e32 v82, 2, v7
	global_load_dwordx2 v[54:55], v[4:5], off offset:32 sc1
	global_load_dwordx2 v[60:61], v[4:5], off offset:288 sc1
	global_load_dwordx2 v[74:75], v[4:5], off offset:40 sc1
	global_load_dwordx2 v[84:85], v[4:5], off offset:296 sc1
	global_load_dwordx2 v[86:87], v[4:5], off offset:48 sc1
	global_load_dwordx2 v[88:89], v[4:5], off offset:304 sc1
	global_load_dwordx2 v[90:91], v[4:5], off offset:56 sc1
	global_load_dwordx2 v[28:29], v[4:5], off offset:312 sc1
	global_load_dwordx2 v[58:59], v[4:5], off offset:64 sc1
	global_load_dwordx2 v[36:37], v[4:5], off offset:320 sc1
	global_load_dwordx2 v[66:67], v[4:5], off offset:72 sc1
	global_load_dwordx2 v[44:45], v[4:5], off offset:328 sc1
	global_load_dwordx2 v[62:63], v[4:5], off offset:80 sc1
	global_load_dwordx2 v[52:53], v[4:5], off offset:336 sc1
	global_load_dwordx2 v[76:77], v[4:5], off offset:88 sc1
	global_load_dwordx2 v[32:33], v[4:5], off offset:344 sc1
	global_load_dwordx2 v[68:69], v[4:5], off offset:96 sc1
	global_load_dwordx2 v[38:39], v[4:5], off offset:352 sc1
	global_load_dwordx2 v[80:81], v[4:5], off offset:104 sc1
	global_load_dwordx2 v[20:21], v[4:5], off offset:360 sc1
	global_load_dwordx2 v[46:47], v[4:5], off offset:112 sc1
	global_load_dwordx2 v[22:23], v[4:5], off offset:368 sc1
	global_load_dwordx2 v[56:57], v[4:5], off offset:120 sc1
	global_load_dwordx2 v[48:49], v[4:5], off offset:376 sc1
	s_nop 0
	global_load_dwordx4 v[4:7], v82, s[58:59] offset:528
	global_load_dwordx4 v[8:11], v82, s[58:59] offset:512
	v_mov_b64_e32 v[14:15], s[16:17]
	v_mad_u64_u32 v[14:15], s[0:1], v12, s5, v[14:15]
	v_mad_i32_i24 v15, v13, s5, v15
	v_lshl_add_u64 v[12:13], v[14:15], 0, v[2:3]
	s_mov_b32 s0, 0xf800000
	s_waitcnt vmcnt(33)
	v_lshlrev_b32_e32 v41, 16, v17
	v_lshlrev_b32_e32 v40, 16, v16
	s_waitcnt vmcnt(32)
	v_lshlrev_b32_e32 v65, 16, v19
	v_lshlrev_b32_e32 v64, 16, v18
	v_and_b32_e32 v17, 0xffff0000, v17
	v_and_b32_e32 v16, 0xffff0000, v16
	v_and_b32_e32 v19, 0xffff0000, v19
	v_and_b32_e32 v18, 0xffff0000, v18
	s_waitcnt vmcnt(29)
	v_lshlrev_b32_e32 v95, 16, v31
	v_lshlrev_b32_e32 v94, 16, v30
	s_waitcnt vmcnt(28)
	v_lshlrev_b32_e32 v97, 16, v35
	v_lshlrev_b32_e32 v96, 16, v34
	v_and_b32_e32 v31, 0xffff0000, v31
	v_and_b32_e32 v30, 0xffff0000, v30
	v_and_b32_e32 v35, 0xffff0000, v35
	v_and_b32_e32 v34, 0xffff0000, v34
	v_pk_fma_f32 v[72:73], v[214:215], v[18:19], v[16:17] neg_lo:[1,0,0] neg_hi:[1,0,0]
	v_pk_fma_f32 v[18:19], v[214:215], v[96:97], v[94:95] neg_lo:[1,0,0] neg_hi:[1,0,0]
	v_pk_fma_f32 v[16:17], v[214:215], v[34:35], v[30:31] neg_lo:[1,0,0] neg_hi:[1,0,0]
	v_lshlrev_b32_e32 v71, 16, v25
	v_lshlrev_b32_e32 v70, 16, v24
	v_lshlrev_b32_e32 v93, 16, v27
	v_lshlrev_b32_e32 v92, 16, v26
	v_and_b32_e32 v25, 0xffff0000, v25
	v_and_b32_e32 v24, 0xffff0000, v24
	v_and_b32_e32 v27, 0xffff0000, v27
	v_and_b32_e32 v26, 0xffff0000, v26
	v_mov_b32_e32 v30, v18
	v_mov_b32_e32 v31, v16
	v_mul_f32_e32 v34, v16, v16
	v_pk_fma_f32 v[78:79], v[214:215], v[64:65], v[40:41] neg_lo:[1,0,0] neg_hi:[1,0,0]
	v_pk_fma_f32 v[64:65], v[214:215], v[26:27], v[24:25] neg_lo:[1,0,0] neg_hi:[1,0,0]
	v_pk_fma_f32 v[30:31], v[30:31], v[30:31], v[34:35] op_sel_hi:[1,1,0]
	v_mov_b32_e32 v34, v19
	v_mov_b32_e32 v35, v17
	v_mul_f32_e32 v40, v17, v17
	v_pk_fma_f32 v[70:71], v[214:215], v[92:93], v[70:71] neg_lo:[1,0,0] neg_hi:[1,0,0]
	v_pk_mul_f32 v[24:25], v[72:73], v[72:73]
	v_pk_mul_f32 v[26:27], v[64:65], v[64:65]
	v_pk_fma_f32 v[34:35], v[34:35], v[34:35], v[40:41] op_sel_hi:[1,1,0]
	s_waitcnt vmcnt(27)
	v_lshlrev_b32_e32 v41, 16, v43
	v_lshlrev_b32_e32 v40, 16, v42
	s_waitcnt vmcnt(26)
	v_lshlrev_b32_e32 v93, 16, v51
	v_lshlrev_b32_e32 v92, 16, v50
	v_and_b32_e32 v43, 0xffff0000, v43
	v_and_b32_e32 v42, 0xffff0000, v42
	v_and_b32_e32 v51, 0xffff0000, v51
	v_and_b32_e32 v50, 0xffff0000, v50
	v_pk_fma_f32 v[24:25], v[78:79], v[78:79], v[24:25]
	v_pk_fma_f32 v[26:27], v[70:71], v[70:71], v[26:27]
	v_pk_fma_f32 v[40:41], v[214:215], v[92:93], v[40:41] neg_lo:[1,0,0] neg_hi:[1,0,0]
	v_pk_fma_f32 v[50:51], v[214:215], v[50:51], v[42:43] neg_lo:[1,0,0] neg_hi:[1,0,0]
	v_pk_add_f32 v[24:25], v[24:25], v[24:25] op_sel:[0,1] op_sel_hi:[1,0]
	v_pk_add_f32 v[26:27], v[26:27], v[26:27] op_sel:[0,1] op_sel_hi:[1,0]
	v_pk_mul_f32 v[42:43], v[40:41], v[40:41]
	v_pk_mul_f32 v[92:93], v[50:51], v[50:51]
	v_mov_b32_e32 v25, v42
	v_mov_b32_e32 v27, v92
	v_mov_b32_e32 v31, v43
	v_mov_b32_e32 v35, v93
	v_pk_add_f32 v[24:25], v[24:25], v[26:27]
	v_pk_add_f32 v[26:27], v[30:31], v[34:35]
	s_waitcnt vmcnt(24)
	v_and_b32_e32 v31, 0xffff0000, v61
	v_pk_add_f32 v[24:25], v[24:25], v[26:27]
	v_lshlrev_b32_e32 v27, 16, v61
	v_pk_add_f32 v[92:93], v[24:25], v[24:25] op_sel:[0,1] op_sel_hi:[1,0]
	v_lshlrev_b32_e32 v25, 16, v55
	v_lshlrev_b32_e32 v24, 16, v54
	v_lshlrev_b32_e32 v26, 16, v60
	v_pk_fma_f32 v[26:27], v[214:215], v[26:27], v[24:25] neg_lo:[1,0,0] neg_hi:[1,0,0]
	v_and_b32_e32 v25, 0xffff0000, v55
	v_and_b32_e32 v24, 0xffff0000, v54
	v_and_b32_e32 v30, 0xffff0000, v60
	v_pk_fma_f32 v[34:35], v[214:215], v[30:31], v[24:25] neg_lo:[1,0,0] neg_hi:[1,0,0]
	s_waitcnt vmcnt(22)
	v_lshlrev_b32_e32 v31, 16, v85
	v_pk_mul_f32 v[24:25], v[34:35], v[34:35]
	v_lshlrev_b32_e32 v30, 16, v84
	v_pk_fma_f32 v[24:25], v[26:27], v[26:27], v[24:25]
	s_waitcnt vmcnt(0)
	v_mov_b32_e32 v15, v10
	v_pk_add_f32 v[60:61], v[24:25], v[24:25] op_sel:[0,1] op_sel_hi:[1,0]
	v_lshlrev_b32_e32 v25, 16, v75
	v_lshlrev_b32_e32 v24, 16, v74
	v_pk_fma_f32 v[42:43], v[214:215], v[30:31], v[24:25] neg_lo:[1,0,0] neg_hi:[1,0,0]
	v_and_b32_e32 v25, 0xffff0000, v75
	v_and_b32_e32 v24, 0xffff0000, v74
	v_and_b32_e32 v31, 0xffff0000, v85
	v_and_b32_e32 v30, 0xffff0000, v84
	v_pk_fma_f32 v[54:55], v[214:215], v[30:31], v[24:25] neg_lo:[1,0,0] neg_hi:[1,0,0]
	v_mov_b32_e32 v24, v42
	v_mov_b32_e32 v25, v54
	v_mul_f32_e32 v30, v54, v54
	v_pk_fma_f32 v[74:75], v[24:25], v[24:25], v[30:31] op_sel_hi:[1,1,0]
	v_mov_b32_e32 v24, v43
	v_mov_b32_e32 v25, v55
	v_mul_f32_e32 v30, v55, v55
	v_pk_fma_f32 v[84:85], v[24:25], v[24:25], v[30:31] op_sel_hi:[1,1,0]
	v_lshlrev_b32_e32 v25, 16, v87
	v_lshlrev_b32_e32 v24, 16, v86
	v_lshlrev_b32_e32 v31, 16, v89
	v_lshlrev_b32_e32 v30, 16, v88
	v_pk_fma_f32 v[24:25], v[214:215], v[30:31], v[24:25] neg_lo:[1,0,0] neg_hi:[1,0,0]
	v_and_b32_e32 v31, 0xffff0000, v87
	v_and_b32_e32 v30, 0xffff0000, v86
	v_and_b32_e32 v87, 0xffff0000, v89
	v_and_b32_e32 v86, 0xffff0000, v88
	v_pk_fma_f32 v[30:31], v[214:215], v[86:87], v[30:31] neg_lo:[1,0,0] neg_hi:[1,0,0]
	v_pk_mul_f32 v[86:87], v[24:25], v[24:25]
	v_pk_mul_f32 v[88:89], v[30:31], v[30:31]
	v_mov_b32_e32 v93, v86
	v_mov_b32_e32 v61, v88
	v_mov_b32_e32 v75, v87
	v_mov_b32_e32 v85, v89
	v_pk_add_f32 v[60:61], v[92:93], v[60:61]
	v_pk_add_f32 v[74:75], v[74:75], v[84:85]
	v_lshlrev_b32_e32 v89, 16, v37
	v_pk_add_f32 v[60:61], v[60:61], v[74:75]
	v_lshlrev_b32_e32 v75, 16, v29
	v_pk_add_f32 v[84:85], v[60:61], v[60:61] op_sel:[0,1] op_sel_hi:[1,0]
	v_lshlrev_b32_e32 v61, 16, v91
	v_lshlrev_b32_e32 v60, 16, v90
	v_lshlrev_b32_e32 v74, 16, v28
	v_pk_fma_f32 v[60:61], v[214:215], v[74:75], v[60:61] neg_lo:[1,0,0] neg_hi:[1,0,0]
	v_and_b32_e32 v75, 0xffff0000, v91
	v_and_b32_e32 v74, 0xffff0000, v90
	v_and_b32_e32 v29, 0xffff0000, v29
	v_and_b32_e32 v28, 0xffff0000, v28
	v_pk_fma_f32 v[74:75], v[214:215], v[28:29], v[74:75] neg_lo:[1,0,0] neg_hi:[1,0,0]
	v_lshlrev_b32_e32 v88, 16, v36
	v_pk_mul_f32 v[28:29], v[74:75], v[74:75]
	v_and_b32_e32 v37, 0xffff0000, v37
	v_pk_fma_f32 v[28:29], v[60:61], v[60:61], v[28:29]
	v_and_b32_e32 v36, 0xffff0000, v36
	v_pk_add_f32 v[86:87], v[28:29], v[28:29] op_sel:[0,1] op_sel_hi:[1,0]
	v_lshlrev_b32_e32 v29, 16, v59
	v_lshlrev_b32_e32 v28, 16, v58
	v_and_b32_e32 v59, 0xffff0000, v59
	v_and_b32_e32 v58, 0xffff0000, v58
	v_pk_fma_f32 v[28:29], v[214:215], v[88:89], v[28:29] neg_lo:[1,0,0] neg_hi:[1,0,0]
	v_pk_fma_f32 v[36:37], v[214:215], v[36:37], v[58:59] neg_lo:[1,0,0] neg_hi:[1,0,0]
	v_mov_b32_e32 v58, v28
	v_mov_b32_e32 v59, v36
	v_mul_f32_e32 v88, v36, v36
	v_pk_fma_f32 v[88:89], v[58:59], v[58:59], v[88:89] op_sel_hi:[1,1,0]
	v_mov_b32_e32 v58, v29
	v_mov_b32_e32 v59, v37
	v_mul_f32_e32 v90, v37, v37
	v_pk_fma_f32 v[90:91], v[58:59], v[58:59], v[90:91] op_sel_hi:[1,1,0]
	v_lshlrev_b32_e32 v59, 16, v67
	v_lshlrev_b32_e32 v58, 16, v66
	v_lshlrev_b32_e32 v93, 16, v45
	v_lshlrev_b32_e32 v92, 16, v44
	v_and_b32_e32 v67, 0xffff0000, v67
	v_and_b32_e32 v66, 0xffff0000, v66
	v_and_b32_e32 v45, 0xffff0000, v45
	v_and_b32_e32 v44, 0xffff0000, v44
	v_pk_fma_f32 v[58:59], v[214:215], v[92:93], v[58:59] neg_lo:[1,0,0] neg_hi:[1,0,0]
	v_pk_fma_f32 v[66:67], v[214:215], v[44:45], v[66:67] neg_lo:[1,0,0] neg_hi:[1,0,0]
	v_pk_mul_f32 v[44:45], v[58:59], v[58:59]
	v_pk_mul_f32 v[92:93], v[66:67], v[66:67]
	v_mov_b32_e32 v85, v44
	v_mov_b32_e32 v87, v92
	v_mov_b32_e32 v89, v45
	v_mov_b32_e32 v91, v93
	v_pk_add_f32 v[84:85], v[84:85], v[86:87]
	v_pk_add_f32 v[44:45], v[88:89], v[90:91]
	v_lshlrev_b32_e32 v87, 16, v53
	v_pk_add_f32 v[44:45], v[84:85], v[44:45]
	v_lshlrev_b32_e32 v86, 16, v52
	v_pk_add_f32 v[84:85], v[44:45], v[44:45] op_sel:[0,1] op_sel_hi:[1,0]
	v_lshlrev_b32_e32 v45, 16, v63
	v_lshlrev_b32_e32 v44, 16, v62
	v_and_b32_e32 v63, 0xffff0000, v63
	v_and_b32_e32 v62, 0xffff0000, v62
	v_and_b32_e32 v53, 0xffff0000, v53
	v_and_b32_e32 v52, 0xffff0000, v52
	v_pk_fma_f32 v[52:53], v[214:215], v[52:53], v[62:63] neg_lo:[1,0,0] neg_hi:[1,0,0]
	v_pk_fma_f32 v[44:45], v[214:215], v[86:87], v[44:45] neg_lo:[1,0,0] neg_hi:[1,0,0]
	v_pk_mul_f32 v[62:63], v[52:53], v[52:53]
	v_lshlrev_b32_e32 v89, 16, v33
	v_pk_fma_f32 v[62:63], v[44:45], v[44:45], v[62:63]
	v_lshlrev_b32_e32 v88, 16, v32
	v_pk_add_f32 v[86:87], v[62:63], v[62:63] op_sel:[0,1] op_sel_hi:[1,0]
	v_lshlrev_b32_e32 v63, 16, v77
	v_lshlrev_b32_e32 v62, 16, v76
	v_and_b32_e32 v77, 0xffff0000, v77
	v_and_b32_e32 v76, 0xffff0000, v76
	v_and_b32_e32 v33, 0xffff0000, v33
	v_and_b32_e32 v32, 0xffff0000, v32
	v_pk_fma_f32 v[62:63], v[214:215], v[88:89], v[62:63] neg_lo:[1,0,0] neg_hi:[1,0,0]
	v_pk_fma_f32 v[76:77], v[214:215], v[32:33], v[76:77] neg_lo:[1,0,0] neg_hi:[1,0,0]
	v_mov_b32_e32 v32, v62
	v_mov_b32_e32 v33, v76
	v_mul_f32_e32 v88, v76, v76
	v_pk_fma_f32 v[88:89], v[32:33], v[32:33], v[88:89] op_sel_hi:[1,1,0]
	v_mov_b32_e32 v32, v63
	v_mov_b32_e32 v33, v77
	v_mul_f32_e32 v90, v77, v77
	v_pk_fma_f32 v[90:91], v[32:33], v[32:33], v[90:91] op_sel_hi:[1,1,0]
	v_lshlrev_b32_e32 v33, 16, v69
	v_lshlrev_b32_e32 v32, 16, v68
	v_lshlrev_b32_e32 v93, 16, v39
	v_lshlrev_b32_e32 v92, 16, v38
	v_and_b32_e32 v69, 0xffff0000, v69
	v_and_b32_e32 v68, 0xffff0000, v68
	v_and_b32_e32 v39, 0xffff0000, v39
	v_and_b32_e32 v38, 0xffff0000, v38
	v_pk_fma_f32 v[32:33], v[214:215], v[92:93], v[32:33] neg_lo:[1,0,0] neg_hi:[1,0,0]
	v_pk_fma_f32 v[38:39], v[214:215], v[38:39], v[68:69] neg_lo:[1,0,0] neg_hi:[1,0,0]
	v_pk_mul_f32 v[68:69], v[32:33], v[32:33]
	v_pk_mul_f32 v[92:93], v[38:39], v[38:39]
	v_mov_b32_e32 v85, v68
	v_mov_b32_e32 v87, v92
	v_mov_b32_e32 v89, v69
	v_mov_b32_e32 v91, v93
	v_pk_add_f32 v[84:85], v[84:85], v[86:87]
	v_pk_add_f32 v[68:69], v[88:89], v[90:91]
	v_lshlrev_b32_e32 v87, 16, v21
	v_pk_add_f32 v[68:69], v[84:85], v[68:69]
	v_lshlrev_b32_e32 v86, 16, v20
	v_pk_add_f32 v[84:85], v[68:69], v[68:69] op_sel:[0,1] op_sel_hi:[1,0]
	v_lshlrev_b32_e32 v69, 16, v81
	v_lshlrev_b32_e32 v68, 16, v80
	v_and_b32_e32 v81, 0xffff0000, v81
	v_and_b32_e32 v80, 0xffff0000, v80
	v_and_b32_e32 v21, 0xffff0000, v21
	v_and_b32_e32 v20, 0xffff0000, v20
	v_pk_fma_f32 v[80:81], v[214:215], v[20:21], v[80:81] neg_lo:[1,0,0] neg_hi:[1,0,0]
	v_pk_fma_f32 v[68:69], v[214:215], v[86:87], v[68:69] neg_lo:[1,0,0] neg_hi:[1,0,0]
	v_pk_mul_f32 v[20:21], v[80:81], v[80:81]
	v_lshlrev_b32_e32 v89, 16, v23
	v_pk_fma_f32 v[20:21], v[68:69], v[68:69], v[20:21]
	v_lshlrev_b32_e32 v88, 16, v22
	v_pk_add_f32 v[86:87], v[20:21], v[20:21] op_sel:[0,1] op_sel_hi:[1,0]
	v_lshlrev_b32_e32 v21, 16, v47
	v_lshlrev_b32_e32 v20, 16, v46
	v_and_b32_e32 v47, 0xffff0000, v47
	v_and_b32_e32 v46, 0xffff0000, v46
	v_and_b32_e32 v23, 0xffff0000, v23
	v_and_b32_e32 v22, 0xffff0000, v22
	v_pk_fma_f32 v[20:21], v[214:215], v[88:89], v[20:21] neg_lo:[1,0,0] neg_hi:[1,0,0]
	v_pk_fma_f32 v[22:23], v[214:215], v[22:23], v[46:47] neg_lo:[1,0,0] neg_hi:[1,0,0]
	v_mov_b32_e32 v46, v20
	v_mov_b32_e32 v47, v22
	v_mul_f32_e32 v88, v22, v22
	v_pk_fma_f32 v[88:89], v[46:47], v[46:47], v[88:89] op_sel_hi:[1,1,0]
	v_mov_b32_e32 v46, v21
	v_mov_b32_e32 v47, v23
	v_mul_f32_e32 v90, v23, v23
	v_pk_fma_f32 v[90:91], v[46:47], v[46:47], v[90:91] op_sel_hi:[1,1,0]
	v_lshlrev_b32_e32 v47, 16, v57
	v_lshlrev_b32_e32 v46, 16, v56
	v_lshlrev_b32_e32 v93, 16, v49
	v_lshlrev_b32_e32 v92, 16, v48
	v_and_b32_e32 v57, 0xffff0000, v57
	v_and_b32_e32 v56, 0xffff0000, v56
	v_and_b32_e32 v49, 0xffff0000, v49
	v_and_b32_e32 v48, 0xffff0000, v48
	v_pk_fma_f32 v[46:47], v[214:215], v[92:93], v[46:47] neg_lo:[1,0,0] neg_hi:[1,0,0]
	v_pk_fma_f32 v[48:49], v[214:215], v[48:49], v[56:57] neg_lo:[1,0,0] neg_hi:[1,0,0]
	v_pk_mul_f32 v[56:57], v[46:47], v[46:47]
	v_pk_mul_f32 v[92:93], v[48:49], v[48:49]
	v_mov_b32_e32 v85, v56
	v_mov_b32_e32 v87, v92
	v_mov_b32_e32 v89, v57
	v_mov_b32_e32 v91, v93
	v_pk_add_f32 v[84:85], v[84:85], v[86:87]
	v_pk_add_f32 v[56:57], v[88:89], v[90:91]
	v_mov_b32_e32 v10, v9
	v_pk_add_f32 v[56:57], v[84:85], v[56:57]
	s_nop 0
	v_add_f32_e32 v56, v56, v57
	ds_bpermute_b32 v57, v83, v56
	s_waitcnt lgkmcnt(0)
	v_add_f32_e32 v2, v56, v57
	v_fmamk_f32 v2, v2, 0x3c000000, v1
	v_mul_f32_e32 v14, 0x4f800000, v2
	v_cmp_gt_f32_e32 vcc, s0, v2
	s_nop 1
	v_cndmask_b32_e32 v2, v2, v14, vcc
	v_sqrt_f32_e32 v56, v2
	v_mov_b32_e32 v14, v8
	v_add_u32_e32 v8, -1, v56
	v_fma_f32 v9, -v8, v56, v2
	v_cmp_ge_f32_e64 s[0:1], 0, v9
	v_add_u32_e32 v9, 1, v56
	s_nop 0
	v_cndmask_b32_e64 v8, v56, v8, s[0:1]
	v_fma_f32 v56, -v9, v56, v2
	v_cmp_lt_f32_e64 s[0:1], 0, v56
	s_nop 1
	v_cndmask_b32_e64 v8, v8, v9, s[0:1]
	v_mul_f32_e32 v9, 0x37800000, v8
	v_cndmask_b32_e32 v8, v8, v9, vcc
	v_cmp_class_f32_e32 vcc, v2, v226
	v_mov_b32_e32 v9, v6
	v_mov_b32_e32 v6, v5
	v_cndmask_b32_e32 v2, v8, v2, vcc
	v_div_scale_f32 v56, s[0:1], v2, v2, 1.0
	v_rcp_f32_e32 v57, v56
	v_mov_b32_e32 v8, v4
	v_fma_f32 v4, -v56, v57, 1.0
	v_fmac_f32_e32 v57, v4, v57
	v_div_scale_f32 v4, vcc, 1.0, v2, 1.0
	v_mul_f32_e32 v5, v4, v57
	v_fma_f32 v83, -v56, v5, v4
	v_fmac_f32_e32 v5, v83, v57
	v_fma_f32 v4, -v56, v5, v4
	v_div_fmas_f32 v4, v4, v57, v5
	v_div_fixup_f32 v2, v4, v2, 1.0
	v_mul_f32_e32 v2, 0x3f24fd5c, v2
	v_pk_mul_f32 v[4:5], v[78:79], v[2:3] op_sel_hi:[1,0]
	v_pk_mul_f32 v[16:17], v[16:17], v[2:3] op_sel_hi:[1,0]
	v_pk_mul_f32 v[4:5], v[14:15], v[4:5]
	v_pk_mul_f32 v[14:15], v[72:73], v[2:3] op_sel_hi:[1,0]
	s_nop 0
	v_pk_mul_f32 v[10:11], v[10:11], v[14:15]
	v_pk_mul_f32 v[14:15], v[70:71], v[2:3] op_sel_hi:[1,0]
	v_pk_mul_f32 v[8:9], v[8:9], v[14:15]
	v_pk_mul_f32 v[14:15], v[64:65], v[2:3] op_sel_hi:[1,0]
	v_pk_mul_f32 v[6:7], v[6:7], v[14:15]
	v_cvt_pk_bf16_f32 v7, v9, v7
	v_cvt_pk_bf16_f32 v6, v8, v6
	v_cvt_pk_bf16_f32 v5, v5, v11
	v_cvt_pk_bf16_f32 v4, v4, v10
	global_store_dwordx4 v[12:13], v[4:7], off offset:1024
	global_load_dwordx4 v[4:7], v82, s[58:59] offset:544
	s_nop 0
	global_load_dwordx4 v[8:11], v82, s[58:59] offset:560
	v_pk_mul_f32 v[14:15], v[18:19], v[2:3] op_sel_hi:[1,0]
	s_waitcnt vmcnt(1)
	v_mov_b32_e32 v19, v6
	v_mov_b32_e32 v6, v5
	v_mov_b32_e32 v18, v4
	v_pk_mul_f32 v[4:5], v[6:7], v[16:17]
	v_pk_mul_f32 v[6:7], v[40:41], v[2:3] op_sel_hi:[1,0]
	s_waitcnt vmcnt(0)
	v_mov_b32_e32 v16, v8
	v_mov_b32_e32 v17, v10
	v_pk_mul_f32 v[6:7], v[16:17], v[6:7]
	v_pk_mul_f32 v[16:17], v[50:51], v[2:3] op_sel_hi:[1,0]
	v_mov_b32_e32 v10, v9
	v_pk_mul_f32 v[8:9], v[10:11], v[16:17]
	v_pk_mul_f32 v[14:15], v[18:19], v[14:15]
	v_bfe_u32 v10, v9, 16, 1
	v_bfe_u32 v11, v8, 16, 1
	v_add3_u32 v8, v8, v11, s62
	v_add3_u32 v9, v9, v10, s62
	v_bfe_u32 v16, v6, 16, 1
	v_bfe_u32 v17, v7, 16, 1
	v_add3_u32 v7, v7, v17, s62
	v_add3_u32 v6, v6, v16, s62
	v_lshrrev_b32_e32 v6, 16, v6
	v_lshrrev_b32_e32 v7, 16, v7
	v_and_or_b32 v7, v9, s61, v7
	v_and_or_b32 v6, v8, s61, v6
	v_cvt_pk_bf16_f32 v5, v15, v5
	v_cvt_pk_bf16_f32 v4, v14, v4
	global_store_dwordx4 v[12:13], v[4:7], off offset:1040
	global_load_dwordx4 v[4:7], v82, s[58:59] offset:576
	s_nop 0
	global_load_dwordx4 v[8:11], v82, s[58:59] offset:592
	v_pk_mul_f32 v[14:15], v[26:27], v[2:3] op_sel_hi:[1,0]
	v_pk_mul_f32 v[18:19], v[62:63], v[2:3] op_sel_hi:[1,0]
	s_waitcnt vmcnt(1)
	v_mov_b32_e32 v16, v4
	v_mov_b32_e32 v17, v6
	v_pk_mul_f32 v[14:15], v[14:15], v[16:17]
	v_pk_mul_f32 v[16:17], v[34:35], v[2:3] op_sel_hi:[1,0]
	v_mov_b32_e32 v6, v5
	v_pk_mul_f32 v[4:5], v[16:17], v[6:7]
	v_pk_mul_f32 v[6:7], v[42:43], v[2:3] op_sel_hi:[1,0]
	s_waitcnt vmcnt(0)
	v_mov_b32_e32 v16, v8
	v_mov_b32_e32 v17, v10
	v_pk_mul_f32 v[6:7], v[6:7], v[16:17]
	v_pk_mul_f32 v[16:17], v[54:55], v[2:3] op_sel_hi:[1,0]
	v_mov_b32_e32 v10, v9
	v_pk_mul_f32 v[8:9], v[16:17], v[10:11]
	v_bfe_u32 v10, v9, 16, 1
	v_bfe_u32 v11, v8, 16, 1
	v_add3_u32 v8, v8, v11, s62
	v_add3_u32 v9, v9, v10, s62
	v_bfe_u32 v16, v6, 16, 1
	v_bfe_u32 v17, v7, 16, 1
	v_add3_u32 v7, v7, v17, s62
	v_add3_u32 v6, v6, v16, s62
	v_lshrrev_b32_e32 v6, 16, v6
	v_lshrrev_b32_e32 v7, 16, v7
	v_and_or_b32 v7, v9, s61, v7
	v_and_or_b32 v6, v8, s61, v6
	v_cvt_pk_bf16_f32 v5, v15, v5
	v_cvt_pk_bf16_f32 v4, v14, v4
	global_store_dwordx4 v[12:13], v[4:7], off offset:1056
	global_load_dwordx4 v[4:7], v82, s[58:59] offset:608
	s_nop 0
	global_load_dwordx4 v[8:11], v82, s[58:59] offset:624
	v_pk_mul_f32 v[14:15], v[24:25], v[2:3] op_sel_hi:[1,0]
	v_pk_mul_f32 v[24:25], v[76:77], v[2:3] op_sel_hi:[1,0]
	s_waitcnt vmcnt(1)
	v_mov_b32_e32 v16, v4
	v_mov_b32_e32 v17, v6
	v_pk_mul_f32 v[14:15], v[14:15], v[16:17]
	v_pk_mul_f32 v[16:17], v[30:31], v[2:3] op_sel_hi:[1,0]
	v_mov_b32_e32 v6, v5
	v_pk_mul_f32 v[4:5], v[16:17], v[6:7]
	v_pk_mul_f32 v[6:7], v[60:61], v[2:3] op_sel_hi:[1,0]
	s_waitcnt vmcnt(0)
	v_mov_b32_e32 v16, v8
	v_mov_b32_e32 v17, v10
	v_pk_mul_f32 v[6:7], v[6:7], v[16:17]
	v_pk_mul_f32 v[16:17], v[74:75], v[2:3] op_sel_hi:[1,0]
	v_mov_b32_e32 v10, v9
	v_pk_mul_f32 v[8:9], v[16:17], v[10:11]
	v_bfe_u32 v10, v9, 16, 1
	v_bfe_u32 v11, v8, 16, 1
	v_add3_u32 v8, v8, v11, s62
	v_add3_u32 v9, v9, v10, s62
	v_bfe_u32 v16, v6, 16, 1
	v_bfe_u32 v17, v7, 16, 1
	v_add3_u32 v7, v7, v17, s62
	v_add3_u32 v6, v6, v16, s62
	v_lshrrev_b32_e32 v6, 16, v6
	v_lshrrev_b32_e32 v7, 16, v7
	v_and_or_b32 v7, v9, s61, v7
	v_and_or_b32 v6, v8, s61, v6
	v_cvt_pk_bf16_f32 v5, v15, v5
	v_cvt_pk_bf16_f32 v4, v14, v4
	global_store_dwordx4 v[12:13], v[4:7], off offset:1072
	global_load_dwordx4 v[4:7], v82, s[58:59] offset:640
	s_nop 0
	global_load_dwordx4 v[8:11], v82, s[58:59] offset:656
	v_pk_mul_f32 v[14:15], v[28:29], v[2:3] op_sel_hi:[1,0]
	s_waitcnt vmcnt(1)
	v_mov_b32_e32 v16, v4
	v_mov_b32_e32 v17, v6
	v_pk_mul_f32 v[14:15], v[14:15], v[16:17]
	v_pk_mul_f32 v[16:17], v[36:37], v[2:3] op_sel_hi:[1,0]
	v_mov_b32_e32 v6, v5
	v_pk_mul_f32 v[4:5], v[16:17], v[6:7]
	v_pk_mul_f32 v[6:7], v[58:59], v[2:3] op_sel_hi:[1,0]
	s_waitcnt vmcnt(0)
	v_mov_b32_e32 v16, v8
	v_mov_b32_e32 v17, v10
	v_pk_mul_f32 v[6:7], v[6:7], v[16:17]
	v_pk_mul_f32 v[16:17], v[66:67], v[2:3] op_sel_hi:[1,0]
	v_mov_b32_e32 v10, v9
	v_pk_mul_f32 v[8:9], v[16:17], v[10:11]
	v_bfe_u32 v10, v9, 16, 1
	v_bfe_u32 v11, v8, 16, 1
	v_add3_u32 v8, v8, v11, s62
	v_add3_u32 v9, v9, v10, s62
	v_bfe_u32 v16, v6, 16, 1
	v_bfe_u32 v17, v7, 16, 1
	v_add3_u32 v7, v7, v17, s62
	v_add3_u32 v6, v6, v16, s62
	v_lshrrev_b32_e32 v6, 16, v6
	v_lshrrev_b32_e32 v7, 16, v7
	v_and_or_b32 v7, v9, s61, v7
	v_and_or_b32 v6, v8, s61, v6
	v_cvt_pk_bf16_f32 v5, v15, v5
	v_cvt_pk_bf16_f32 v4, v14, v4
	global_store_dwordx4 v[12:13], v[4:7], off offset:1088
	global_load_dwordx4 v[4:7], v82, s[58:59] offset:672
	s_nop 0
	global_load_dwordx4 v[8:11], v82, s[58:59] offset:688
	v_pk_mul_f32 v[16:17], v[52:53], v[2:3] op_sel_hi:[1,0]
	v_pk_mul_f32 v[14:15], v[44:45], v[2:3] op_sel_hi:[1,0]
	s_waitcnt vmcnt(1)
	v_mov_b32_e32 v27, v6
	v_mov_b32_e32 v6, v5
	s_waitcnt vmcnt(0)
	v_mov_b32_e32 v5, v10
	v_mov_b32_e32 v10, v9
	v_mov_b32_e32 v26, v4
	v_mov_b32_e32 v4, v8
	v_pk_mul_f32 v[6:7], v[16:17], v[6:7]
	v_pk_mul_f32 v[10:11], v[24:25], v[10:11]
	v_pk_mul_f32 v[8:9], v[14:15], v[26:27]
	v_pk_mul_f32 v[4:5], v[18:19], v[4:5]
	v_bfe_u32 v14, v11, 16, 1
	v_bfe_u32 v15, v10, 16, 1
	v_bfe_u32 v16, v7, 16, 1
	v_bfe_u32 v17, v6, 16, 1
	v_add3_u32 v17, v6, v17, s62
	v_add3_u32 v16, v7, v16, s62
	v_add3_u32 v6, v10, v15, s62
	v_add3_u32 v7, v11, v14, s62
	v_bfe_u32 v10, v8, 16, 1
	v_bfe_u32 v11, v9, 16, 1
	v_bfe_u32 v14, v4, 16, 1
	v_bfe_u32 v15, v5, 16, 1
	v_add3_u32 v5, v5, v15, s62
	v_add3_u32 v4, v4, v14, s62
	v_add3_u32 v9, v9, v11, s62
	v_add3_u32 v8, v8, v10, s62
	v_lshrrev_b32_e32 v8, 16, v8
	v_lshrrev_b32_e32 v9, 16, v9
	v_lshrrev_b32_e32 v4, 16, v4
	v_lshrrev_b32_e32 v5, 16, v5
	v_and_or_b32 v7, v7, s61, v5
	v_and_or_b32 v6, v6, s61, v4
	v_and_or_b32 v5, v16, s61, v9
	v_and_or_b32 v4, v17, s61, v8
	global_store_dwordx4 v[12:13], v[4:7], off offset:1104
	global_load_dwordx4 v[4:7], v82, s[58:59] offset:704
	s_nop 0
	global_load_dwordx4 v[8:11], v82, s[58:59] offset:720
	v_pk_mul_f32 v[14:15], v[32:33], v[2:3] op_sel_hi:[1,0]
	v_pk_mul_f32 v[18:19], v[68:69], v[2:3] op_sel_hi:[1,0]
	v_pk_mul_f32 v[16:17], v[38:39], v[2:3] op_sel_hi:[1,0]
	v_pk_mul_f32 v[24:25], v[80:81], v[2:3] op_sel_hi:[1,0]
	s_waitcnt vmcnt(1)
	v_mov_b32_e32 v26, v4
	v_mov_b32_e32 v27, v6
	v_mov_b32_e32 v6, v5
	s_waitcnt vmcnt(0)
	v_mov_b32_e32 v4, v8
	v_mov_b32_e32 v5, v10
	v_mov_b32_e32 v10, v9
	v_pk_mul_f32 v[8:9], v[14:15], v[26:27]
	v_pk_mul_f32 v[4:5], v[18:19], v[4:5]
	v_pk_mul_f32 v[6:7], v[16:17], v[6:7]
	v_pk_mul_f32 v[10:11], v[24:25], v[10:11]
	v_bfe_u32 v18, v8, 16, 1
	v_bfe_u32 v19, v9, 16, 1
	v_bfe_u32 v16, v7, 16, 1
	v_bfe_u32 v17, v6, 16, 1
	v_add3_u32 v9, v9, v19, s62
	v_add3_u32 v8, v8, v18, s62
	v_add3_u32 v17, v6, v17, s62
	v_add3_u32 v16, v7, v16, s62
	v_lshrrev_b32_e32 v8, 16, v8
	v_lshrrev_b32_e32 v9, 16, v9
	v_cvt_pk_bf16_f32 v7, v5, v11
	v_cvt_pk_bf16_f32 v6, v4, v10
	v_and_or_b32 v5, v16, s61, v9
	v_and_or_b32 v4, v17, s61, v8
	global_store_dwordx4 v[12:13], v[4:7], off offset:1120
	global_load_dwordx4 v[4:7], v82, s[58:59] offset:736
	s_nop 0
	global_load_dwordx4 v[8:11], v82, s[58:59] offset:752
	v_pk_mul_f32 v[14:15], v[20:21], v[2:3] op_sel_hi:[1,0]
	v_pk_mul_f32 v[16:17], v[22:23], v[2:3] op_sel_hi:[1,0]
	v_pk_mul_f32 v[18:19], v[46:47], v[2:3] op_sel_hi:[1,0]
	v_pk_mul_f32 v[20:21], v[48:49], v[2:3] op_sel_hi:[1,0]
	s_waitcnt vmcnt(1)
	v_mov_b32_e32 v22, v4
	v_mov_b32_e32 v23, v6
	v_mov_b32_e32 v6, v5
	s_waitcnt vmcnt(0)
	v_mov_b32_e32 v4, v8
	v_mov_b32_e32 v5, v10
	v_mov_b32_e32 v10, v9
	v_pk_mul_f32 v[8:9], v[14:15], v[22:23]
	v_pk_mul_f32 v[6:7], v[16:17], v[6:7]
	v_pk_mul_f32 v[4:5], v[18:19], v[4:5]
	v_pk_mul_f32 v[10:11], v[20:21], v[10:11]
	v_bfe_u32 v15, v7, 16, 1
	v_bfe_u32 v17, v8, 16, 1
	v_bfe_u32 v18, v9, 16, 1
	v_bfe_u32 v19, v4, 16, 1
	v_bfe_u32 v14, v10, 16, 1
	v_bfe_u32 v16, v6, 16, 1
	v_add3_u32 v15, v7, v15, s62
	v_add3_u32 v4, v4, v19, s62
	v_add3_u32 v7, v9, v18, s62
	v_add3_u32 v8, v8, v17, s62
	v_add3_u32 v16, v6, v16, s62
	v_add3_u32 v6, v10, v14, s62
	v_lshrrev_b32_e32 v8, 16, v8
	v_lshrrev_b32_e32 v9, 16, v7
	v_lshrrev_b32_e32 v4, 16, v4
	v_cvt_pk_bf16_f32 v7, v5, v11
	v_and_or_b32 v6, v6, s61, v4
	v_and_or_b32 v5, v15, s61, v9
	v_and_or_b32 v4, v16, s61, v8
	global_store_dwordx4 v[12:13], v[4:7], off offset:1136
	s_branch .LBB0_872
